# K-loops: the back-to-back s_setprio 0 / s_setprio 1 between the two 8-MFMA groups of a phase removed (one priority window per phase), on top of load-early
# baseline (speedup 1.0000x reference)
.LBB0_194:
	s_add_u32 s34, s92, 0xfffa0080
	s_addc_u32 s35, s93, -1
	s_add_i32 s2, 0, 0x10000
	s_cmp_eq_u32 s1, 12
	s_cselect_b32 s95, s57, s35
	s_cselect_b32 s94, vcc_lo, s34
	s_cselect_b32 s97, s55, s11
	s_cselect_b32 s96, vcc_hi, s10
	s_add_i32 s82, 0, 0x14000
	s_mov_b32 s34, 0xfffe0000
	s_mov_b32 s35, -1
	v_lshl_add_u64 v[168:169], s[92:93], 0, v[154:155]
	v_lshl_add_u64 v[168:169], v[168:169], 0, s[34:35]
	s_add_i32 m0, s89, 0xc000
	s_nop 0
	global_load_lds_dwordx4 v[168:169], off
	s_add_i32 m0, s89, 0xe000
	s_nop 0
	global_load_lds_dwordx4 v154, s[92:93]
	v_add_u32_e32 v146, s68, v174
	v_add_u32_e32 v142, s2, v146
	v_add_u32_e32 v164, s82, v146
	ds_read_b128 v[130:133], v142
	ds_read_b128 v[134:137], v142 offset:1024
	ds_read_b128 v[138:141], v142 offset:2048
	ds_read_b128 v[142:145], v142 offset:3072
	ds_read_b128 v[146:149], v164
	ds_read_b128 v[150:153], v164 offset:1024
	ds_read_b128 v[160:163], v164 offset:2048
	ds_read_b128 v[164:167], v164 offset:3072
	v_add_u32_e32 v159, s69, v174
	ds_read_b128 v[176:179], v159
	ds_read_b128 v[180:183], v159 offset:1024
	ds_read_b128 v[184:187], v159 offset:2048
	ds_read_b128 v[188:191], v159 offset:3072
	ds_read_b128 v[196:199], v159 offset:4096
	ds_read_b128 v[200:203], v159 offset:5120
	ds_read_b128 v[204:207], v159 offset:6144
	ds_read_b128 v[208:211], v159 offset:7168
	s_waitcnt vmcnt(8)
	s_waitcnt lgkmcnt(0)
	s_barrier
	s_setprio 1
	s_waitcnt lgkmcnt(0)
	v_mfma_scale_f32_16x16x128_f8f6f4 v[126:129], v[130:137], v[176:183], v[126:129], v1, v1 op_sel_hi:[0,0,0]
	v_mfma_scale_f32_16x16x128_f8f6f4 v[122:125], v[138:145], v[176:183], v[122:125], v1, v1 op_sel_hi:[0,0,0]
	v_mfma_scale_f32_16x16x128_f8f6f4 v[114:117], v[130:137], v[184:191], v[114:117], v1, v1 op_sel_hi:[0,0,0]
	v_mfma_scale_f32_16x16x128_f8f6f4 v[106:109], v[138:145], v[184:191], v[106:109], v1, v1 op_sel_hi:[0,0,0]
	v_mfma_scale_f32_16x16x128_f8f6f4 v[98:101], v[130:137], v[196:203], v[98:101], v1, v1 op_sel_hi:[0,0,0]
	v_mfma_scale_f32_16x16x128_f8f6f4 v[212:215], v[138:145], v[196:203], v[90:93], v1, v1 op_sel_hi:[0,0,0]
	v_mfma_scale_f32_16x16x128_f8f6f4 v[216:219], v[130:137], v[204:211], v[82:85], v1, v1 op_sel_hi:[0,0,0]
	v_mfma_scale_f32_16x16x128_f8f6f4 v[220:223], v[138:145], v[204:211], v[74:77], v1, v1 op_sel_hi:[0,0,0]
	v_mfma_scale_f32_16x16x128_f8f6f4 v[118:121], v[146:153], v[176:183], v[118:121], v1, v1 op_sel_hi:[0,0,0]
	v_mfma_scale_f32_16x16x128_f8f6f4 v[110:113], v[160:167], v[176:183], v[110:113], v1, v1 op_sel_hi:[0,0,0]
	v_mfma_scale_f32_16x16x128_f8f6f4 v[102:105], v[146:153], v[184:191], v[102:105], v1, v1 op_sel_hi:[0,0,0]
	v_mfma_scale_f32_16x16x128_f8f6f4 v[176:179], v[160:167], v[184:191], v[94:97], v1, v1 op_sel_hi:[0,0,0]
	v_mfma_scale_f32_16x16x128_f8f6f4 v[180:183], v[146:153], v[196:203], v[86:89], v1, v1 op_sel_hi:[0,0,0]
	v_mfma_scale_f32_16x16x128_f8f6f4 v[184:187], v[160:167], v[196:203], v[78:81], v1, v1 op_sel_hi:[0,0,0]
	v_mfma_scale_f32_16x16x128_f8f6f4 v[188:191], v[146:153], v[204:211], v[62:65], v1, v1 op_sel_hi:[0,0,0]
	v_mfma_scale_f32_16x16x128_f8f6f4 v[196:199], v[160:167], v[204:211], v[58:61], v1, v1 op_sel_hi:[0,0,0]
	s_setprio 0
	s_barrier
	v_mov_b32_e32 v159, v155
	v_add_u32_e32 v94, s69, v174
	s_add_i32 s2, s2, s6
	s_nop 1
	s_mov_b32 m0, s2
	v_lshl_add_u64 v[168:169], s[96:97], 0, v[158:159]
	global_load_lds_dwordx4 v158, s[96:97]
	v_lshl_add_u64 v[168:169], v[168:169], 0, s[14:15]
	s_add_i32 m0, s2, 0x2000
	s_add_i32 s2, s82, s6
	global_load_lds_dwordx4 v[168:169], off
	s_mov_b32 m0, s2
	v_lshl_add_u64 v[168:169], s[96:97], 0, v[158:159]
	v_lshl_add_u64 v[170:171], v[168:169], 0, s[16:17]
	global_load_lds_dwordx4 v[170:171], off
	v_lshl_add_u64 v[168:169], v[168:169], 0, s[18:19]
	s_add_i32 m0, s2, 0x2000
	s_nop 0
	global_load_lds_dwordx4 v[168:169], off
	s_mov_b32 m0, s89
	v_lshl_add_u64 v[168:169], s[94:95], 0, v[154:155]
	global_load_lds_dwordx4 v154, s[94:95]
	v_lshl_add_u64 v[168:169], v[168:169], 0, s[14:15]
	s_mov_b32 m0, s91
	s_nop 0
	global_load_lds_dwordx4 v[168:169], off
	ds_read_b128 v[58:61], v94 offset:16384
	ds_read_b128 v[62:65], v94 offset:17408
	ds_read_b128 v[74:77], v94 offset:18432
	ds_read_b128 v[78:81], v94 offset:19456
	ds_read_b128 v[82:85], v94 offset:20480
	ds_read_b128 v[86:89], v94 offset:21504
	ds_read_b128 v[90:93], v94 offset:22528
	ds_read_b128 v[94:97], v94 offset:23552
	s_waitcnt vmcnt(8)
	s_waitcnt lgkmcnt(0)
	s_barrier
	s_setprio 1
	s_waitcnt lgkmcnt(0)
	v_mfma_scale_f32_16x16x128_f8f6f4 v[54:57], v[130:137], v[58:65], v[54:57], v1, v1 op_sel_hi:[0,0,0]
	v_mfma_scale_f32_16x16x128_f8f6f4 v[200:203], v[138:145], v[58:65], v[42:45], v1, v1 op_sel_hi:[0,0,0]
	v_mfma_scale_f32_16x16x128_f8f6f4 v[204:207], v[130:137], v[74:81], v[30:33], v1, v1 op_sel_hi:[0,0,0]
	v_mfma_scale_f32_16x16x128_f8f6f4 v[208:211], v[138:145], v[74:81], v[26:29], v1, v1 op_sel_hi:[0,0,0]
	v_mfma_scale_f32_16x16x128_f8f6f4 v[224:227], v[130:137], v[82:89], v[14:17], v1, v1 op_sel_hi:[0,0,0]
	v_mfma_scale_f32_16x16x128_f8f6f4 v[228:231], v[138:145], v[82:89], v[10:13], v1, v1 op_sel_hi:[0,0,0]
	v_mfma_scale_f32_16x16x128_f8f6f4 v[232:235], v[130:137], v[90:97], v[6:9], v1, v1 op_sel_hi:[0,0,0]
	v_mfma_scale_f32_16x16x128_f8f6f4 v[236:239], v[138:145], v[90:97], v[2:5], v1, v1 op_sel_hi:[0,0,0]
	v_mfma_scale_f32_16x16x128_f8f6f4 v[66:69], v[146:153], v[58:65], v[66:69], v1, v1 op_sel_hi:[0,0,0]
	v_mfma_scale_f32_16x16x128_f8f6f4 v[70:73], v[160:167], v[58:65], v[70:73], v1, v1 op_sel_hi:[0,0,0]
	v_mfma_scale_f32_16x16x128_f8f6f4 v[50:53], v[160:167], v[74:81], v[50:53], v1, v1 op_sel_hi:[0,0,0]
	v_mfma_scale_f32_16x16x128_f8f6f4 v[240:243], v[146:153], v[74:81], v[46:49], v1, v1 op_sel_hi:[0,0,0]
	v_mfma_scale_f32_16x16x128_f8f6f4 v[244:247], v[146:153], v[82:89], v[34:37], v1, v1 op_sel_hi:[0,0,0]
	v_mfma_scale_f32_16x16x128_f8f6f4 v[248:251], v[160:167], v[82:89], v[38:41], v1, v1 op_sel_hi:[0,0,0]
	v_mfma_scale_f32_16x16x128_f8f6f4 v[192:195], v[146:153], v[90:97], v[18:21], v1, v1 op_sel_hi:[0,0,0]
	v_mfma_scale_f32_16x16x128_f8f6f4 v[168:171], v[160:167], v[90:97], v[22:25], v1, v1 op_sel_hi:[0,0,0]
	s_setprio 0
	s_barrier
	s_mov_b32 m0, s7
	v_lshl_add_u64 v[58:59], s[94:95], 0, v[154:155]
	v_lshl_add_u64 v[60:61], v[58:59], 0, s[16:17]
	global_load_lds_dwordx4 v[60:61], off
	v_lshl_add_u64 v[58:59], v[58:59], 0, s[18:19]
	s_mov_b32 m0, s0
	s_nop 0
	global_load_lds_dwordx4 v[58:59], off
	s_add_i32 s2, 0, 0x18000
	v_add_u32_e32 v10, s68, v174
	s_add_i32 s34, 0, 0x1c000
	v_add_u32_e32 v22, s2, v10
	v_add_u32_e32 v10, s34, v10
	ds_read_b128 v[2:5], v22
	ds_read_b128 v[6:9], v22 offset:1024
	ds_read_b128 v[18:21], v22 offset:2048
	ds_read_b128 v[22:25], v22 offset:3072
	ds_read_b128 v[130:133], v10
	ds_read_b128 v[134:137], v10 offset:1024
	ds_read_b128 v[138:141], v10 offset:2048
	ds_read_b128 v[142:145], v10 offset:3072
	v_add_u32_e32 v46, s69, v174
	ds_read_b128 v[10:13], v46 offset:32768
	ds_read_b128 v[14:17], v46 offset:33792
	ds_read_b128 v[26:29], v46 offset:34816
	ds_read_b128 v[30:33], v46 offset:35840
	ds_read_b128 v[34:37], v46 offset:36864
	ds_read_b128 v[38:41], v46 offset:37888
	ds_read_b128 v[42:45], v46 offset:38912
	ds_read_b128 v[46:49], v46 offset:39936
	s_waitcnt vmcnt(8)
	s_waitcnt lgkmcnt(0)
	s_barrier
	s_setprio 1
	s_waitcnt lgkmcnt(0)
	v_mfma_scale_f32_16x16x128_f8f6f4 v[126:129], v[2:9], v[10:17], v[126:129], v1, v1 op_sel_hi:[0,0,0]
	v_mfma_scale_f32_16x16x128_f8f6f4 v[122:125], v[18:25], v[10:17], v[122:125], v1, v1 op_sel_hi:[0,0,0]
	v_mfma_scale_f32_16x16x128_f8f6f4 v[114:117], v[2:9], v[26:33], v[114:117], v1, v1 op_sel_hi:[0,0,0]
	v_mfma_scale_f32_16x16x128_f8f6f4 v[106:109], v[18:25], v[26:33], v[106:109], v1, v1 op_sel_hi:[0,0,0]
	v_mfma_scale_f32_16x16x128_f8f6f4 v[98:101], v[2:9], v[34:41], v[98:101], v1, v1 op_sel_hi:[0,0,0]
	v_mfma_scale_f32_16x16x128_f8f6f4 v[90:93], v[18:25], v[34:41], v[212:215], v1, v1 op_sel_hi:[0,0,0]
	v_mfma_scale_f32_16x16x128_f8f6f4 v[82:85], v[2:9], v[42:49], v[216:219], v1, v1 op_sel_hi:[0,0,0]
	v_mfma_scale_f32_16x16x128_f8f6f4 v[74:77], v[18:25], v[42:49], v[220:223], v1, v1 op_sel_hi:[0,0,0]
	v_mfma_scale_f32_16x16x128_f8f6f4 v[118:121], v[130:137], v[10:17], v[118:121], v1, v1 op_sel_hi:[0,0,0]
	v_mfma_scale_f32_16x16x128_f8f6f4 v[110:113], v[138:145], v[10:17], v[110:113], v1, v1 op_sel_hi:[0,0,0]
	v_mfma_scale_f32_16x16x128_f8f6f4 v[102:105], v[130:137], v[26:33], v[102:105], v1, v1 op_sel_hi:[0,0,0]
	v_mfma_scale_f32_16x16x128_f8f6f4 v[94:97], v[138:145], v[26:33], v[176:179], v1, v1 op_sel_hi:[0,0,0]
	v_mfma_scale_f32_16x16x128_f8f6f4 v[86:89], v[130:137], v[34:41], v[180:183], v1, v1 op_sel_hi:[0,0,0]
	v_mfma_scale_f32_16x16x128_f8f6f4 v[78:81], v[138:145], v[34:41], v[184:187], v1, v1 op_sel_hi:[0,0,0]
	v_mfma_scale_f32_16x16x128_f8f6f4 v[62:65], v[130:137], v[42:49], v[188:191], v1, v1 op_sel_hi:[0,0,0]
	v_mfma_scale_f32_16x16x128_f8f6f4 v[58:61], v[138:145], v[42:49], v[196:199], v1, v1 op_sel_hi:[0,0,0]
	s_setprio 0
	s_barrier
	s_add_i32 s2, s2, s6
	s_mov_b32 m0, s2
	v_lshl_add_u64 v[10:11], s[96:97], 0, v[158:159]
	v_lshl_add_u64 v[12:13], v[10:11], 0, s[20:21]
	global_load_lds_dwordx4 v[12:13], off
	v_lshl_add_u64 v[10:11], v[10:11], 0, s[22:23]
	s_add_i32 m0, s2, 0x2000
	s_add_i32 s2, s34, s6
	global_load_lds_dwordx4 v[10:11], off
	s_mov_b32 m0, s2
	v_lshl_add_u64 v[10:11], s[96:97], 0, v[158:159]
	v_lshl_add_u64 v[12:13], v[10:11], 0, s[24:25]
	global_load_lds_dwordx4 v[12:13], off
	v_lshl_add_u64 v[10:11], v[10:11], 0, s[26:27]
	s_add_i32 m0, s2, 0x2000
	s_nop 0
	global_load_lds_dwordx4 v[10:11], off
	s_mov_b32 m0, s33
	v_lshl_add_u64 v[10:11], s[94:95], 0, v[154:155]
	v_lshl_add_u64 v[12:13], v[10:11], 0, s[20:21]
	global_load_lds_dwordx4 v[12:13], off
	v_lshl_add_u64 v[10:11], v[10:11], 0, s[22:23]
	s_mov_b32 m0, s76
	s_nop 0
	global_load_lds_dwordx4 v[10:11], off
	v_add_u32_e32 v180, s69, v174
	ds_read_b128 v[34:37], v180 offset:49152
	ds_read_b128 v[38:41], v180 offset:50176
	ds_read_b128 v[146:149], v180 offset:51200
	ds_read_b128 v[150:153], v180 offset:52224
	ds_read_b128 v[160:163], v180 offset:53248
	ds_read_b128 v[164:167], v180 offset:54272
	ds_read_b128 v[176:179], v180 offset:55296
	ds_read_b128 v[180:183], v180 offset:56320
	s_waitcnt vmcnt(8)
	s_waitcnt lgkmcnt(0)
	s_barrier
	s_setprio 1
	s_waitcnt lgkmcnt(0)
	v_mfma_scale_f32_16x16x128_f8f6f4 v[54:57], v[2:9], v[34:41], v[54:57], v1, v1 op_sel_hi:[0,0,0]
	v_mfma_scale_f32_16x16x128_f8f6f4 v[42:45], v[18:25], v[34:41], v[200:203], v1, v1 op_sel_hi:[0,0,0]
	v_mfma_scale_f32_16x16x128_f8f6f4 v[30:33], v[2:9], v[146:153], v[204:207], v1, v1 op_sel_hi:[0,0,0]
	v_mfma_scale_f32_16x16x128_f8f6f4 v[26:29], v[18:25], v[146:153], v[208:211], v1, v1 op_sel_hi:[0,0,0]
	v_mfma_scale_f32_16x16x128_f8f6f4 v[14:17], v[2:9], v[160:167], v[224:227], v1, v1 op_sel_hi:[0,0,0]
	v_mfma_scale_f32_16x16x128_f8f6f4 v[10:13], v[18:25], v[160:167], v[228:231], v1, v1 op_sel_hi:[0,0,0]
	v_mfma_scale_f32_16x16x128_f8f6f4 v[6:9], v[2:9], v[176:183], v[232:235], v1, v1 op_sel_hi:[0,0,0]
	v_mfma_scale_f32_16x16x128_f8f6f4 v[2:5], v[18:25], v[176:183], v[236:239], v1, v1 op_sel_hi:[0,0,0]
	v_mfma_scale_f32_16x16x128_f8f6f4 v[66:69], v[130:137], v[34:41], v[66:69], v1, v1 op_sel_hi:[0,0,0]
	v_mfma_scale_f32_16x16x128_f8f6f4 v[70:73], v[138:145], v[34:41], v[70:73], v1, v1 op_sel_hi:[0,0,0]
	v_mfma_scale_f32_16x16x128_f8f6f4 v[46:49], v[130:137], v[146:153], v[240:243], v1, v1 op_sel_hi:[0,0,0]
	v_mfma_scale_f32_16x16x128_f8f6f4 v[50:53], v[138:145], v[146:153], v[50:53], v1, v1 op_sel_hi:[0,0,0]
	v_mfma_scale_f32_16x16x128_f8f6f4 v[34:37], v[130:137], v[160:167], v[244:247], v1, v1 op_sel_hi:[0,0,0]
	v_mfma_scale_f32_16x16x128_f8f6f4 v[38:41], v[138:145], v[160:167], v[248:251], v1, v1 op_sel_hi:[0,0,0]
	v_mfma_scale_f32_16x16x128_f8f6f4 v[18:21], v[130:137], v[176:183], v[192:195], v1, v1 op_sel_hi:[0,0,0]
	v_mfma_scale_f32_16x16x128_f8f6f4 v[22:25], v[138:145], v[176:183], v[168:171], v1, v1 op_sel_hi:[0,0,0]
	s_setprio 0
	s_barrier
	s_add_i32 s1, s1, 2
	s_add_u32 s92, s92, 0x100
	s_addc_u32 s93, s93, 0
	s_add_u32 s10, s10, 0x100
	s_addc_u32 s11, s11, 0
	s_cmp_gt_u32 s1, 13
	s_cbranch_scc0 .LBB0_194
	s_and_b64 vcc, exec, s[64:65]
	s_cbranch_vccz .LBB0_197
	s_barrier

.LBB0_977:
	s_add_u32 s34, s58, 0xfffd0080
	v_add_u32_e32 v46, s84, v1
	v_add_u32_e32 v142, s88, v46
	v_add_u32_e32 v46, s89, v46
	ds_read_b128 v[130:133], v142
	ds_read_b128 v[134:137], v142 offset:1024
	ds_read_b128 v[138:141], v142 offset:2048
	ds_read_b128 v[142:145], v142 offset:3072
	ds_read_b128 v[146:149], v46
	ds_read_b128 v[150:153], v46 offset:1024
	ds_read_b128 v[154:157], v46 offset:2048
	ds_read_b128 v[158:161], v46 offset:3072
	s_addc_u32 s35, s59, -1
	s_cmp_eq_u32 s70, 4
	s_cselect_b32 s61, s38, s35
	s_cselect_b32 s60, s39, s34
	s_cselect_b32 s63, s45, s69
	s_cselect_b32 s62, s47, s68
	s_mov_b32 s34, 0xffff0000
	s_mov_b32 s35, -1
	v_lshl_add_u64 v[46:47], s[58:59], 0, v[196:197]
	v_lshl_add_u64 v[46:47], v[46:47], 0, s[34:35]
	s_add_i32 m0, s64, 0xc000
	s_nop 0
	global_load_lds_dwordx4 v[46:47], off
	s_add_i32 m0, s64, 0xe000
	s_nop 0
	global_load_lds_dwordx4 v196, s[58:59]
	v_add_u32_e32 v190, s85, v1
	ds_read_b128 v[162:165], v190
	ds_read_b128 v[166:169], v190 offset:1024
	ds_read_b128 v[170:173], v190 offset:2048
	ds_read_b128 v[174:177], v190 offset:3072
	ds_read_b128 v[178:181], v190 offset:4096
	ds_read_b128 v[182:185], v190 offset:5120
	ds_read_b128 v[186:189], v190 offset:6144
	ds_read_b128 v[190:193], v190 offset:7168
	s_waitcnt vmcnt(8)
	s_waitcnt lgkmcnt(0)
	s_barrier
	s_setprio 1
	s_waitcnt lgkmcnt(0)
	v_mfma_scale_f32_16x16x128_f8f6f4 v[94:97], v[130:137], v[162:169], v[94:97], v195, v195 op_sel_hi:[0,0,0]
	v_mfma_scale_f32_16x16x128_f8f6f4 v[90:93], v[138:145], v[162:169], v[90:93], v195, v195 op_sel_hi:[0,0,0]
	v_mfma_scale_f32_16x16x128_f8f6f4 v[86:89], v[130:137], v[170:177], v[86:89], v195, v195 op_sel_hi:[0,0,0]
	v_mfma_scale_f32_16x16x128_f8f6f4 v[82:85], v[138:145], v[170:177], v[82:85], v195, v195 op_sel_hi:[0,0,0]
	v_mfma_scale_f32_16x16x128_f8f6f4 v[78:81], v[130:137], v[178:185], v[78:81], v195, v195 op_sel_hi:[0,0,0]
	v_mfma_scale_f32_16x16x128_f8f6f4 v[204:207], v[138:145], v[178:185], v[74:77], v195, v195 op_sel_hi:[0,0,0]
	v_mfma_scale_f32_16x16x128_f8f6f4 v[208:211], v[130:137], v[186:193], v[70:73], v195, v195 op_sel_hi:[0,0,0]
	v_mfma_scale_f32_16x16x128_f8f6f4 v[212:215], v[138:145], v[186:193], v[66:69], v195, v195 op_sel_hi:[0,0,0]
	v_mfma_scale_f32_16x16x128_f8f6f4 v[38:41], v[154:161], v[178:185], v[38:41], v195, v195 op_sel_hi:[0,0,0]
	v_mfma_scale_f32_16x16x128_f8f6f4 v[216:219], v[146:153], v[162:169], v[62:65], v195, v195 op_sel_hi:[0,0,0]
	v_mfma_scale_f32_16x16x128_f8f6f4 v[162:165], v[154:161], v[162:169], v[58:61], v195, v195 op_sel_hi:[0,0,0]
	v_mfma_scale_f32_16x16x128_f8f6f4 v[166:169], v[146:153], v[170:177], v[54:57], v195, v195 op_sel_hi:[0,0,0]
	v_mfma_scale_f32_16x16x128_f8f6f4 v[170:173], v[154:161], v[170:177], v[14:17], v195, v195 op_sel_hi:[0,0,0]
	v_mfma_scale_f32_16x16x128_f8f6f4 v[174:177], v[146:153], v[178:185], v[10:13], v195, v195 op_sel_hi:[0,0,0]
	v_mfma_scale_f32_16x16x128_f8f6f4 v[178:181], v[146:153], v[186:193], v[30:33], v195, v195 op_sel_hi:[0,0,0]
	v_mfma_scale_f32_16x16x128_f8f6f4 v[182:185], v[154:161], v[186:193], v[22:25], v195, v195 op_sel_hi:[0,0,0]
	s_setprio 0
	s_barrier
	v_mov_b32_e32 v203, v197
	s_nop 1
	s_add_i32 s34, s88, s43
	s_mov_b32 m0, s34
	v_lshl_add_u64 v[10:11], s[62:63], 0, v[202:203]
	global_load_lds_dwordx4 v202, s[62:63]
	v_lshl_add_u64 v[10:11], v[10:11], 0, s[12:13]
	s_add_i32 m0, s34, 0x2000
	s_add_i32 s34, s89, s43
	global_load_lds_dwordx4 v[10:11], off
	s_mov_b32 m0, s34
	v_lshl_add_u64 v[10:11], s[62:63], 0, v[202:203]
	v_lshl_add_u64 v[12:13], v[10:11], 0, s[14:15]
	global_load_lds_dwordx4 v[12:13], off
	v_lshl_add_u64 v[10:11], v[10:11], 0, s[16:17]
	s_add_i32 m0, s34, 0x2000
	s_nop 0
	global_load_lds_dwordx4 v[10:11], off
	s_mov_b32 m0, s64
	v_lshl_add_u64 v[10:11], s[60:61], 0, v[196:197]
	global_load_lds_dwordx4 v196, s[60:61]
	v_lshl_add_u64 v[10:11], v[10:11], 0, s[12:13]
	s_mov_b32 m0, s65
	s_nop 0
	global_load_lds_dwordx4 v[10:11], off
	v_add_u32_e32 v74, s85, v1
	ds_read_b128 v[46:49], v74 offset:16384
	ds_read_b128 v[50:53], v74 offset:17408
	ds_read_b128 v[54:57], v74 offset:18432
	ds_read_b128 v[58:61], v74 offset:19456
	ds_read_b128 v[62:65], v74 offset:20480
	ds_read_b128 v[66:69], v74 offset:21504
	ds_read_b128 v[70:73], v74 offset:22528
	ds_read_b128 v[74:77], v74 offset:23552
	s_waitcnt vmcnt(8)
	s_waitcnt lgkmcnt(0)
	s_barrier
	s_setprio 1
	s_waitcnt lgkmcnt(0)
	v_mfma_scale_f32_16x16x128_f8f6f4 v[42:45], v[130:137], v[46:53], v[42:45], v195, v195 op_sel_hi:[0,0,0]
	v_mfma_scale_f32_16x16x128_f8f6f4 v[34:37], v[138:145], v[46:53], v[34:37], v195, v195 op_sel_hi:[0,0,0]
	v_mfma_scale_f32_16x16x128_f8f6f4 v[224:227], v[130:137], v[62:69], v[224:227], v195, v195 op_sel_hi:[0,0,0]
	v_mfma_scale_f32_16x16x128_f8f6f4 v[228:231], v[138:145], v[62:69], v[228:231], v195, v195 op_sel_hi:[0,0,0]
	v_mfma_scale_f32_16x16x128_f8f6f4 v[186:189], v[130:137], v[54:61], v[26:29], v195, v195 op_sel_hi:[0,0,0]
	v_mfma_scale_f32_16x16x128_f8f6f4 v[190:193], v[138:145], v[54:61], v[18:21], v195, v195 op_sel_hi:[0,0,0]
	v_mfma_scale_f32_16x16x128_f8f6f4 v[232:235], v[130:137], v[70:77], v[6:9], v195, v195 op_sel_hi:[0,0,0]
	v_mfma_scale_f32_16x16x128_f8f6f4 v[236:239], v[138:145], v[70:77], v[2:5], v195, v195 op_sel_hi:[0,0,0]
	v_mfma_scale_f32_16x16x128_f8f6f4 v[240:243], v[146:153], v[46:53], v[98:101], v195, v195 op_sel_hi:[0,0,0]
	v_mfma_scale_f32_16x16x128_f8f6f4 v[244:247], v[154:161], v[46:53], v[102:105], v195, v195 op_sel_hi:[0,0,0]
	v_mfma_scale_f32_16x16x128_f8f6f4 v[248:251], v[146:153], v[54:61], v[106:109], v195, v195 op_sel_hi:[0,0,0]
	v_mfma_scale_f32_16x16x128_f8f6f4 v[198:201], v[154:161], v[54:61], v[110:113], v195, v195 op_sel_hi:[0,0,0]
	v_mfma_scale_f32_16x16x128_f8f6f4 v[220:223], v[146:153], v[62:69], v[114:117], v195, v195 op_sel_hi:[0,0,0]
	v_mfma_scale_f32_16x16x128_f8f6f4 v[46:49], v[154:161], v[62:69], v[118:121], v195, v195 op_sel_hi:[0,0,0]
	v_mfma_scale_f32_16x16x128_f8f6f4 v[50:53], v[146:153], v[70:77], v[122:125], v195, v195 op_sel_hi:[0,0,0]
	v_mfma_scale_f32_16x16x128_f8f6f4 v[154:157], v[154:161], v[70:77], v[126:129], v195, v195 op_sel_hi:[0,0,0]
	s_setprio 0
	s_barrier
	s_mov_b32 m0, s66
	v_lshl_add_u64 v[54:55], s[60:61], 0, v[196:197]
	v_lshl_add_u64 v[56:57], v[54:55], 0, s[14:15]
	global_load_lds_dwordx4 v[56:57], off
	v_lshl_add_u64 v[54:55], v[54:55], 0, s[16:17]
	s_mov_b32 m0, s67
	s_nop 0
	global_load_lds_dwordx4 v[54:55], off
	s_add_i32 s34, 0, 0x18000
	v_add_u32_e32 v10, s84, v1
	s_add_i32 s35, 0, 0x1c000
	v_add_u32_e32 v102, s34, v10
	v_add_u32_e32 v10, s35, v10
	ds_read_b128 v[2:5], v102
	ds_read_b128 v[6:9], v102 offset:1024
	ds_read_b128 v[98:101], v102 offset:2048
	ds_read_b128 v[102:105], v102 offset:3072
	ds_read_b128 v[122:125], v10
	ds_read_b128 v[126:129], v10 offset:1024
	ds_read_b128 v[130:133], v10 offset:2048
	ds_read_b128 v[134:137], v10 offset:3072
	v_add_u32_e32 v110, s85, v1
	ds_read_b128 v[10:13], v110 offset:32768
	ds_read_b128 v[14:17], v110 offset:33792
	ds_read_b128 v[18:21], v110 offset:34816
	ds_read_b128 v[22:25], v110 offset:35840
	ds_read_b128 v[26:29], v110 offset:36864
	ds_read_b128 v[30:33], v110 offset:37888
	ds_read_b128 v[106:109], v110 offset:38912
	ds_read_b128 v[110:113], v110 offset:39936
	s_waitcnt vmcnt(8)
	s_waitcnt lgkmcnt(0)
	s_barrier
	s_setprio 1
	s_waitcnt lgkmcnt(0)
	v_mfma_scale_f32_16x16x128_f8f6f4 v[94:97], v[2:9], v[10:17], v[94:97], v195, v195 op_sel_hi:[0,0,0]
	v_mfma_scale_f32_16x16x128_f8f6f4 v[90:93], v[98:105], v[10:17], v[90:93], v195, v195 op_sel_hi:[0,0,0]
	v_mfma_scale_f32_16x16x128_f8f6f4 v[86:89], v[2:9], v[18:25], v[86:89], v195, v195 op_sel_hi:[0,0,0]
	v_mfma_scale_f32_16x16x128_f8f6f4 v[82:85], v[98:105], v[18:25], v[82:85], v195, v195 op_sel_hi:[0,0,0]
	v_mfma_scale_f32_16x16x128_f8f6f4 v[78:81], v[2:9], v[26:33], v[78:81], v195, v195 op_sel_hi:[0,0,0]
	v_mfma_scale_f32_16x16x128_f8f6f4 v[74:77], v[98:105], v[26:33], v[204:207], v195, v195 op_sel_hi:[0,0,0]
	v_mfma_scale_f32_16x16x128_f8f6f4 v[70:73], v[2:9], v[106:113], v[208:211], v195, v195 op_sel_hi:[0,0,0]
	v_mfma_scale_f32_16x16x128_f8f6f4 v[66:69], v[98:105], v[106:113], v[212:215], v195, v195 op_sel_hi:[0,0,0]
	v_mfma_scale_f32_16x16x128_f8f6f4 v[62:65], v[122:129], v[10:17], v[216:219], v195, v195 op_sel_hi:[0,0,0]
	v_mfma_scale_f32_16x16x128_f8f6f4 v[58:61], v[130:137], v[10:17], v[162:165], v195, v195 op_sel_hi:[0,0,0]
	v_mfma_scale_f32_16x16x128_f8f6f4 v[54:57], v[122:129], v[18:25], v[166:169], v195, v195 op_sel_hi:[0,0,0]
	v_mfma_scale_f32_16x16x128_f8f6f4 v[14:17], v[130:137], v[18:25], v[170:173], v195, v195 op_sel_hi:[0,0,0]
	v_mfma_scale_f32_16x16x128_f8f6f4 v[10:13], v[122:129], v[26:33], v[174:177], v195, v195 op_sel_hi:[0,0,0]
	v_mfma_scale_f32_16x16x128_f8f6f4 v[38:41], v[130:137], v[26:33], v[38:41], v195, v195 op_sel_hi:[0,0,0]
	v_mfma_scale_f32_16x16x128_f8f6f4 v[30:33], v[122:129], v[106:113], v[178:181], v195, v195 op_sel_hi:[0,0,0]
	v_mfma_scale_f32_16x16x128_f8f6f4 v[22:25], v[130:137], v[106:113], v[182:185], v195, v195 op_sel_hi:[0,0,0]
	s_setprio 0
	s_barrier
	s_add_i32 s34, s34, s43
	s_mov_b32 m0, s34
	v_lshl_add_u64 v[18:19], s[62:63], 0, v[202:203]
	v_lshl_add_u64 v[20:21], v[18:19], 0, s[24:25]
	global_load_lds_dwordx4 v[20:21], off
	v_lshl_add_u64 v[18:19], v[18:19], 0, s[26:27]
	s_add_i32 m0, s34, 0x2000
	s_add_i32 s34, s35, s43
	global_load_lds_dwordx4 v[18:19], off
	s_mov_b32 m0, s34
	v_lshl_add_u64 v[18:19], s[62:63], 0, v[202:203]
	v_lshl_add_u64 v[20:21], v[18:19], 0, s[28:29]
	global_load_lds_dwordx4 v[20:21], off
	v_lshl_add_u64 v[18:19], v[18:19], 0, s[30:31]
	s_add_i32 m0, s34, 0x2000
	s_nop 0
	global_load_lds_dwordx4 v[18:19], off
	s_mov_b32 m0, s82
	v_lshl_add_u64 v[18:19], s[60:61], 0, v[196:197]
	v_lshl_add_u64 v[20:21], v[18:19], 0, s[24:25]
	global_load_lds_dwordx4 v[20:21], off
	v_lshl_add_u64 v[18:19], v[18:19], 0, s[26:27]
	s_mov_b32 m0, s83
	s_nop 0
	global_load_lds_dwordx4 v[18:19], off
	v_add_u32_e32 v150, s85, v1
	ds_read_b128 v[106:109], v150 offset:49152
	ds_read_b128 v[110:113], v150 offset:50176
	ds_read_b128 v[114:117], v150 offset:51200
	ds_read_b128 v[118:121], v150 offset:52224
	ds_read_b128 v[138:141], v150 offset:53248
	ds_read_b128 v[142:145], v150 offset:54272
	ds_read_b128 v[146:149], v150 offset:55296
	ds_read_b128 v[150:153], v150 offset:56320
	s_waitcnt vmcnt(8)
	s_waitcnt lgkmcnt(0)
	s_barrier
	s_setprio 1
	s_waitcnt lgkmcnt(0)
	v_mfma_scale_f32_16x16x128_f8f6f4 v[42:45], v[2:9], v[106:113], v[42:45], v195, v195 op_sel_hi:[0,0,0]
	v_mfma_scale_f32_16x16x128_f8f6f4 v[34:37], v[98:105], v[106:113], v[34:37], v195, v195 op_sel_hi:[0,0,0]
	v_mfma_scale_f32_16x16x128_f8f6f4 v[26:29], v[2:9], v[114:121], v[186:189], v195, v195 op_sel_hi:[0,0,0]
	v_mfma_scale_f32_16x16x128_f8f6f4 v[18:21], v[98:105], v[114:121], v[190:193], v195, v195 op_sel_hi:[0,0,0]
	v_mfma_scale_f32_16x16x128_f8f6f4 v[224:227], v[2:9], v[138:145], v[224:227], v195, v195 op_sel_hi:[0,0,0]
	v_mfma_scale_f32_16x16x128_f8f6f4 v[228:231], v[98:105], v[138:145], v[228:231], v195, v195 op_sel_hi:[0,0,0]
	v_mfma_scale_f32_16x16x128_f8f6f4 v[6:9], v[2:9], v[146:153], v[232:235], v195, v195 op_sel_hi:[0,0,0]
	v_mfma_scale_f32_16x16x128_f8f6f4 v[2:5], v[98:105], v[146:153], v[236:239], v195, v195 op_sel_hi:[0,0,0]
	v_mfma_scale_f32_16x16x128_f8f6f4 v[98:101], v[122:129], v[106:113], v[240:243], v195, v195 op_sel_hi:[0,0,0]
	v_mfma_scale_f32_16x16x128_f8f6f4 v[102:105], v[130:137], v[106:113], v[244:247], v195, v195 op_sel_hi:[0,0,0]
	v_mfma_scale_f32_16x16x128_f8f6f4 v[106:109], v[122:129], v[114:121], v[248:251], v195, v195 op_sel_hi:[0,0,0]
	v_mfma_scale_f32_16x16x128_f8f6f4 v[110:113], v[130:137], v[114:121], v[198:201], v195, v195 op_sel_hi:[0,0,0]
	v_mfma_scale_f32_16x16x128_f8f6f4 v[114:117], v[122:129], v[138:145], v[220:223], v195, v195 op_sel_hi:[0,0,0]
	v_mfma_scale_f32_16x16x128_f8f6f4 v[118:121], v[130:137], v[138:145], v[46:49], v195, v195 op_sel_hi:[0,0,0]
	v_mfma_scale_f32_16x16x128_f8f6f4 v[122:125], v[122:129], v[146:153], v[50:53], v195, v195 op_sel_hi:[0,0,0]
	v_mfma_scale_f32_16x16x128_f8f6f4 v[126:129], v[130:137], v[146:153], v[154:157], v195, v195 op_sel_hi:[0,0,0]
	s_setprio 0
	s_barrier
	s_add_i32 s70, s70, 2
	s_add_u32 s58, s58, 0x100
	s_addc_u32 s59, s59, 0
	s_add_u32 s68, s68, 0x100
	s_addc_u32 s69, s69, 0
	s_cmp_gt_u32 s70, 5
	s_cbranch_scc0 .LBB0_977
	s_and_b64 vcc, exec, s[36:37]
	s_cbranch_vccz .LBB0_980
	s_barrier

.LBB0_1074:
	s_add_u32 s2, s54, 0xfffa0080
	s_addc_u32 s34, s55, -1
	s_cmp_eq_u32 s76, 12
	s_cselect_b32 s57, s38, s34
	s_cselect_b32 s56, s39, s2
	s_cselect_b32 s59, s41, s75
	s_cselect_b32 s58, s43, s74
	s_mov_b32 s34, 0xfffe0000
	s_mov_b32 s35, -1
	v_lshl_add_u64 v[154:155], s[54:55], 0, v[158:159]
	v_lshl_add_u64 v[154:155], v[154:155], 0, s[34:35]
	s_add_i32 m0, s51, 0xc000
	s_nop 0
	global_load_lds_dwordx4 v[154:155], off
	s_add_i32 m0, s51, 0xe000
	s_nop 0
	global_load_lds_dwordx4 v158, s[54:55]
	v_add_u32_e32 v146, s66, v1
	v_add_u32_e32 v142, s71, v146
	v_add_u32_e32 v176, s72, v146
	ds_read_b128 v[130:133], v142
	ds_read_b128 v[134:137], v142 offset:1024
	ds_read_b128 v[138:141], v142 offset:2048
	ds_read_b128 v[142:145], v142 offset:3072
	ds_read_b128 v[146:149], v176
	ds_read_b128 v[150:153], v176 offset:1024
	ds_read_b128 v[172:175], v176 offset:2048
	ds_read_b128 v[176:179], v176 offset:3072
	v_add_u32_e32 v216, s67, v1
	ds_read_b128 v[180:183], v216
	ds_read_b128 v[184:187], v216 offset:1024
	ds_read_b128 v[196:199], v216 offset:2048
	ds_read_b128 v[200:203], v216 offset:3072
	ds_read_b128 v[204:207], v216 offset:4096
	ds_read_b128 v[208:211], v216 offset:5120
	ds_read_b128 v[212:215], v216 offset:6144
	ds_read_b128 v[216:219], v216 offset:7168
	s_waitcnt vmcnt(8)
	s_waitcnt lgkmcnt(0)
	s_barrier
	s_setprio 1
	s_waitcnt lgkmcnt(0)
	v_mfma_scale_f32_16x16x128_f8f6f4 v[126:129], v[130:137], v[180:187], v[126:129], v170, v170 op_sel_hi:[0,0,0]
	v_mfma_scale_f32_16x16x128_f8f6f4 v[122:125], v[138:145], v[180:187], v[122:125], v170, v170 op_sel_hi:[0,0,0]
	v_mfma_scale_f32_16x16x128_f8f6f4 v[114:117], v[130:137], v[196:203], v[114:117], v170, v170 op_sel_hi:[0,0,0]
	v_mfma_scale_f32_16x16x128_f8f6f4 v[106:109], v[138:145], v[196:203], v[106:109], v170, v170 op_sel_hi:[0,0,0]
	v_mfma_scale_f32_16x16x128_f8f6f4 v[98:101], v[130:137], v[204:211], v[98:101], v170, v170 op_sel_hi:[0,0,0]
	v_mfma_scale_f32_16x16x128_f8f6f4 v[154:157], v[138:145], v[204:211], v[90:93], v170, v170 op_sel_hi:[0,0,0]
	v_mfma_scale_f32_16x16x128_f8f6f4 v[166:169], v[130:137], v[212:219], v[82:85], v170, v170 op_sel_hi:[0,0,0]
	v_mfma_scale_f32_16x16x128_f8f6f4 v[188:191], v[138:145], v[212:219], v[74:77], v170, v170 op_sel_hi:[0,0,0]
	v_mfma_scale_f32_16x16x128_f8f6f4 v[118:121], v[146:153], v[180:187], v[118:121], v170, v170 op_sel_hi:[0,0,0]
	v_mfma_scale_f32_16x16x128_f8f6f4 v[110:113], v[172:179], v[180:187], v[110:113], v170, v170 op_sel_hi:[0,0,0]
	v_mfma_scale_f32_16x16x128_f8f6f4 v[102:105], v[146:153], v[196:203], v[102:105], v170, v170 op_sel_hi:[0,0,0]
	v_mfma_scale_f32_16x16x128_f8f6f4 v[180:183], v[172:179], v[196:203], v[94:97], v170, v170 op_sel_hi:[0,0,0]
	v_mfma_scale_f32_16x16x128_f8f6f4 v[184:187], v[146:153], v[204:211], v[86:89], v170, v170 op_sel_hi:[0,0,0]
	v_mfma_scale_f32_16x16x128_f8f6f4 v[192:195], v[172:179], v[204:211], v[78:81], v170, v170 op_sel_hi:[0,0,0]
	v_mfma_scale_f32_16x16x128_f8f6f4 v[196:199], v[146:153], v[212:219], v[70:73], v170, v170 op_sel_hi:[0,0,0]
	v_mfma_scale_f32_16x16x128_f8f6f4 v[200:203], v[172:179], v[212:219], v[66:69], v170, v170 op_sel_hi:[0,0,0]
	s_setprio 0
	s_barrier
	v_mov_b32_e32 v165, v159
	v_add_u32_e32 v94, s67, v1
	s_add_i32 s2, s71, s37
	s_nop 1
	s_mov_b32 m0, s2
	v_lshl_add_u64 v[204:205], s[58:59], 0, v[164:165]
	global_load_lds_dwordx4 v164, s[58:59]
	v_lshl_add_u64 v[204:205], v[204:205], 0, s[12:13]
	s_add_i32 m0, s2, 0x2000
	s_add_i32 s2, s72, s37
	global_load_lds_dwordx4 v[204:205], off
	s_mov_b32 m0, s2
	v_lshl_add_u64 v[204:205], s[58:59], 0, v[164:165]
	v_lshl_add_u64 v[206:207], v[204:205], 0, s[14:15]
	global_load_lds_dwordx4 v[206:207], off
	v_lshl_add_u64 v[204:205], v[204:205], 0, s[16:17]
	s_add_i32 m0, s2, 0x2000
	s_nop 0
	global_load_lds_dwordx4 v[204:205], off
	s_mov_b32 m0, s51
	v_lshl_add_u64 v[204:205], s[56:57], 0, v[158:159]
	global_load_lds_dwordx4 v158, s[56:57]
	v_lshl_add_u64 v[204:205], v[204:205], 0, s[12:13]
	s_mov_b32 m0, s60
	s_nop 0
	global_load_lds_dwordx4 v[204:205], off
	ds_read_b128 v[66:69], v94 offset:16384
	ds_read_b128 v[70:73], v94 offset:17408
	ds_read_b128 v[74:77], v94 offset:18432
	ds_read_b128 v[78:81], v94 offset:19456
	ds_read_b128 v[82:85], v94 offset:20480
	ds_read_b128 v[86:89], v94 offset:21504
	ds_read_b128 v[90:93], v94 offset:22528
	ds_read_b128 v[94:97], v94 offset:23552
	s_waitcnt vmcnt(8)
	s_waitcnt lgkmcnt(0)
	s_barrier
	s_setprio 1
	s_waitcnt lgkmcnt(0)
	v_mfma_scale_f32_16x16x128_f8f6f4 v[54:57], v[130:137], v[66:73], v[54:57], v170, v170 op_sel_hi:[0,0,0]
	v_mfma_scale_f32_16x16x128_f8f6f4 v[18:21], v[130:137], v[82:89], v[18:21], v170, v170 op_sel_hi:[0,0,0]
	v_mfma_scale_f32_16x16x128_f8f6f4 v[204:207], v[138:145], v[66:73], v[50:53], v170, v170 op_sel_hi:[0,0,0]
	v_mfma_scale_f32_16x16x128_f8f6f4 v[208:211], v[130:137], v[74:81], v[38:41], v170, v170 op_sel_hi:[0,0,0]
	v_mfma_scale_f32_16x16x128_f8f6f4 v[212:215], v[138:145], v[74:81], v[30:33], v170, v170 op_sel_hi:[0,0,0]
	v_mfma_scale_f32_16x16x128_f8f6f4 v[216:219], v[138:145], v[82:89], v[10:13], v170, v170 op_sel_hi:[0,0,0]
	v_mfma_scale_f32_16x16x128_f8f6f4 v[220:223], v[130:137], v[90:97], v[6:9], v170, v170 op_sel_hi:[0,0,0]
	v_mfma_scale_f32_16x16x128_f8f6f4 v[224:227], v[138:145], v[90:97], v[2:5], v170, v170 op_sel_hi:[0,0,0]
	v_mfma_scale_f32_16x16x128_f8f6f4 v[62:65], v[146:153], v[66:73], v[62:65], v170, v170 op_sel_hi:[0,0,0]
	v_mfma_scale_f32_16x16x128_f8f6f4 v[58:61], v[172:179], v[66:73], v[58:61], v170, v170 op_sel_hi:[0,0,0]
	v_mfma_scale_f32_16x16x128_f8f6f4 v[228:231], v[146:153], v[74:81], v[46:49], v170, v170 op_sel_hi:[0,0,0]
	v_mfma_scale_f32_16x16x128_f8f6f4 v[232:235], v[172:179], v[74:81], v[42:45], v170, v170 op_sel_hi:[0,0,0]
	v_mfma_scale_f32_16x16x128_f8f6f4 v[236:239], v[146:153], v[82:89], v[34:37], v170, v170 op_sel_hi:[0,0,0]
	v_mfma_scale_f32_16x16x128_f8f6f4 v[240:243], v[172:179], v[82:89], v[26:29], v170, v170 op_sel_hi:[0,0,0]
	v_mfma_scale_f32_16x16x128_f8f6f4 v[244:247], v[146:153], v[90:97], v[22:25], v170, v170 op_sel_hi:[0,0,0]
	v_mfma_scale_f32_16x16x128_f8f6f4 v[248:251], v[172:179], v[90:97], v[14:17], v170, v170 op_sel_hi:[0,0,0]
	s_setprio 0
	s_barrier
	s_mov_b32 m0, s61
	v_lshl_add_u64 v[66:67], s[56:57], 0, v[158:159]
	v_lshl_add_u64 v[68:69], v[66:67], 0, s[14:15]
	global_load_lds_dwordx4 v[68:69], off
	v_lshl_add_u64 v[66:67], v[66:67], 0, s[16:17]
	s_mov_b32 m0, s62
	s_nop 0
	global_load_lds_dwordx4 v[66:67], off
	s_add_i32 s2, 0, 0x18000
	v_add_u32_e32 v10, s66, v1
	s_add_i32 s34, 0, 0x1c000
	v_add_u32_e32 v26, s2, v10
	v_add_u32_e32 v10, s34, v10
	ds_read_b128 v[2:5], v26
	ds_read_b128 v[6:9], v26 offset:1024
	ds_read_b128 v[22:25], v26 offset:2048
	ds_read_b128 v[26:29], v26 offset:3072
	ds_read_b128 v[130:133], v10
	ds_read_b128 v[134:137], v10 offset:1024
	ds_read_b128 v[138:141], v10 offset:2048
	ds_read_b128 v[142:145], v10 offset:3072
	v_add_u32_e32 v50, s67, v1
	ds_read_b128 v[10:13], v50 offset:32768
	ds_read_b128 v[14:17], v50 offset:33792
	ds_read_b128 v[30:33], v50 offset:34816
	ds_read_b128 v[34:37], v50 offset:35840
	ds_read_b128 v[38:41], v50 offset:36864
	ds_read_b128 v[42:45], v50 offset:37888
	ds_read_b128 v[46:49], v50 offset:38912
	ds_read_b128 v[50:53], v50 offset:39936
	s_waitcnt vmcnt(8)
	s_waitcnt lgkmcnt(0)
	s_barrier
	s_setprio 1
	s_waitcnt lgkmcnt(0)
	v_mfma_scale_f32_16x16x128_f8f6f4 v[126:129], v[2:9], v[10:17], v[126:129], v170, v170 op_sel_hi:[0,0,0]
	v_mfma_scale_f32_16x16x128_f8f6f4 v[122:125], v[22:29], v[10:17], v[122:125], v170, v170 op_sel_hi:[0,0,0]
	v_mfma_scale_f32_16x16x128_f8f6f4 v[114:117], v[2:9], v[30:37], v[114:117], v170, v170 op_sel_hi:[0,0,0]
	v_mfma_scale_f32_16x16x128_f8f6f4 v[106:109], v[22:29], v[30:37], v[106:109], v170, v170 op_sel_hi:[0,0,0]
	v_mfma_scale_f32_16x16x128_f8f6f4 v[98:101], v[2:9], v[38:45], v[98:101], v170, v170 op_sel_hi:[0,0,0]
	v_mfma_scale_f32_16x16x128_f8f6f4 v[90:93], v[22:29], v[38:45], v[154:157], v170, v170 op_sel_hi:[0,0,0]
	v_mfma_scale_f32_16x16x128_f8f6f4 v[82:85], v[2:9], v[46:53], v[166:169], v170, v170 op_sel_hi:[0,0,0]
	v_mfma_scale_f32_16x16x128_f8f6f4 v[74:77], v[22:29], v[46:53], v[188:191], v170, v170 op_sel_hi:[0,0,0]
	v_mfma_scale_f32_16x16x128_f8f6f4 v[118:121], v[130:137], v[10:17], v[118:121], v170, v170 op_sel_hi:[0,0,0]
	v_mfma_scale_f32_16x16x128_f8f6f4 v[110:113], v[138:145], v[10:17], v[110:113], v170, v170 op_sel_hi:[0,0,0]
	v_mfma_scale_f32_16x16x128_f8f6f4 v[102:105], v[130:137], v[30:37], v[102:105], v170, v170 op_sel_hi:[0,0,0]
	v_mfma_scale_f32_16x16x128_f8f6f4 v[94:97], v[138:145], v[30:37], v[180:183], v170, v170 op_sel_hi:[0,0,0]
	v_mfma_scale_f32_16x16x128_f8f6f4 v[86:89], v[130:137], v[38:45], v[184:187], v170, v170 op_sel_hi:[0,0,0]
	v_mfma_scale_f32_16x16x128_f8f6f4 v[78:81], v[138:145], v[38:45], v[192:195], v170, v170 op_sel_hi:[0,0,0]
	v_mfma_scale_f32_16x16x128_f8f6f4 v[70:73], v[130:137], v[46:53], v[196:199], v170, v170 op_sel_hi:[0,0,0]
	v_mfma_scale_f32_16x16x128_f8f6f4 v[66:69], v[138:145], v[46:53], v[200:203], v170, v170 op_sel_hi:[0,0,0]
	s_setprio 0
	s_barrier
	s_add_i32 s2, s2, s37
	s_mov_b32 m0, s2
	v_lshl_add_u64 v[10:11], s[58:59], 0, v[164:165]
	v_lshl_add_u64 v[12:13], v[10:11], 0, s[22:23]
	global_load_lds_dwordx4 v[12:13], off
	v_lshl_add_u64 v[10:11], v[10:11], 0, s[24:25]
	s_add_i32 m0, s2, 0x2000
	s_add_i32 s2, s34, s37
	global_load_lds_dwordx4 v[10:11], off
	s_mov_b32 m0, s2
	v_lshl_add_u64 v[10:11], s[58:59], 0, v[164:165]
	v_lshl_add_u64 v[12:13], v[10:11], 0, s[26:27]
	global_load_lds_dwordx4 v[12:13], off
	v_lshl_add_u64 v[10:11], v[10:11], 0, s[28:29]
	s_add_i32 m0, s2, 0x2000
	s_nop 0
	global_load_lds_dwordx4 v[10:11], off
	s_mov_b32 m0, s64
	v_lshl_add_u64 v[10:11], s[56:57], 0, v[158:159]
	v_lshl_add_u64 v[12:13], v[10:11], 0, s[22:23]
	global_load_lds_dwordx4 v[12:13], off
	v_lshl_add_u64 v[10:11], v[10:11], 0, s[24:25]
	s_mov_b32 m0, s65
	s_nop 0
	global_load_lds_dwordx4 v[10:11], off
	v_add_u32_e32 v184, s67, v1
	ds_read_b128 v[42:45], v184 offset:49152
	ds_read_b128 v[46:49], v184 offset:50176
	ds_read_b128 v[146:149], v184 offset:51200
	ds_read_b128 v[150:153], v184 offset:52224
	ds_read_b128 v[172:175], v184 offset:53248
	ds_read_b128 v[176:179], v184 offset:54272
	ds_read_b128 v[180:183], v184 offset:55296
	ds_read_b128 v[184:187], v184 offset:56320
	s_waitcnt vmcnt(8)
	s_waitcnt lgkmcnt(0)
	s_barrier
	s_setprio 1
	s_waitcnt lgkmcnt(0)
	v_mfma_scale_f32_16x16x128_f8f6f4 v[54:57], v[2:9], v[42:49], v[54:57], v170, v170 op_sel_hi:[0,0,0]
	v_mfma_scale_f32_16x16x128_f8f6f4 v[50:53], v[22:29], v[42:49], v[204:207], v170, v170 op_sel_hi:[0,0,0]
	v_mfma_scale_f32_16x16x128_f8f6f4 v[38:41], v[2:9], v[146:153], v[208:211], v170, v170 op_sel_hi:[0,0,0]
	v_mfma_scale_f32_16x16x128_f8f6f4 v[30:33], v[22:29], v[146:153], v[212:215], v170, v170 op_sel_hi:[0,0,0]
	v_mfma_scale_f32_16x16x128_f8f6f4 v[18:21], v[2:9], v[172:179], v[18:21], v170, v170 op_sel_hi:[0,0,0]
	v_mfma_scale_f32_16x16x128_f8f6f4 v[10:13], v[22:29], v[172:179], v[216:219], v170, v170 op_sel_hi:[0,0,0]
	v_mfma_scale_f32_16x16x128_f8f6f4 v[6:9], v[2:9], v[180:187], v[220:223], v170, v170 op_sel_hi:[0,0,0]
	v_mfma_scale_f32_16x16x128_f8f6f4 v[2:5], v[22:29], v[180:187], v[224:227], v170, v170 op_sel_hi:[0,0,0]
	v_mfma_scale_f32_16x16x128_f8f6f4 v[62:65], v[130:137], v[42:49], v[62:65], v170, v170 op_sel_hi:[0,0,0]
	v_mfma_scale_f32_16x16x128_f8f6f4 v[58:61], v[138:145], v[42:49], v[58:61], v170, v170 op_sel_hi:[0,0,0]
	v_mfma_scale_f32_16x16x128_f8f6f4 v[46:49], v[130:137], v[146:153], v[228:231], v170, v170 op_sel_hi:[0,0,0]
	v_mfma_scale_f32_16x16x128_f8f6f4 v[42:45], v[138:145], v[146:153], v[232:235], v170, v170 op_sel_hi:[0,0,0]
	v_mfma_scale_f32_16x16x128_f8f6f4 v[34:37], v[130:137], v[172:179], v[236:239], v170, v170 op_sel_hi:[0,0,0]
	v_mfma_scale_f32_16x16x128_f8f6f4 v[26:29], v[138:145], v[172:179], v[240:243], v170, v170 op_sel_hi:[0,0,0]
	v_mfma_scale_f32_16x16x128_f8f6f4 v[22:25], v[130:137], v[180:187], v[244:247], v170, v170 op_sel_hi:[0,0,0]
	v_mfma_scale_f32_16x16x128_f8f6f4 v[14:17], v[138:145], v[180:187], v[248:251], v170, v170 op_sel_hi:[0,0,0]
	s_setprio 0
	s_barrier
	s_add_i32 s76, s76, 2
	s_add_u32 s54, s54, 0x100
	s_addc_u32 s55, s55, 0
	s_add_u32 s74, s74, 0x100
	s_addc_u32 s75, s75, 0
	s_cmp_gt_u32 s76, 13
	s_cbranch_scc0 .LBB0_1074
	s_and_b64 vcc, exec, s[30:31]
	s_cbranch_vccz .LBB0_1077
	s_barrier

.LBB0_1224:
	s_add_u32 s64, s46, s58
	v_add_u32_e32 v42, s76, v1
	v_add_u32_e32 v152, s79, v42
	v_add_u32_e32 v42, s81, v42
	ds_read_b128 v[140:143], v152
	ds_read_b128 v[144:147], v152 offset:1024
	ds_read_b128 v[148:151], v152 offset:2048
	ds_read_b128 v[152:155], v152 offset:3072
	ds_read_b128 v[156:159], v42
	ds_read_b128 v[160:163], v42 offset:1024
	ds_read_b128 v[164:167], v42 offset:2048
	ds_read_b128 v[168:171], v42 offset:3072
	s_addc_u32 s65, s47, s59
	s_add_u32 s34, s64, 0x100
	s_addc_u32 s35, s65, 0
	s_add_u32 s62, s2, s58
	s_addc_u32 s63, s49, s59
	s_cmpk_eq_i32 s58, 0x700
	s_cselect_b32 s61, s55, s35
	s_cselect_b32 s60, s54, s34
	s_cselect_b32 s63, s57, s63
	s_cselect_b32 s62, s56, s62
	s_add_i32 m0, s27, 0xc000
	v_lshl_add_u64 v[42:43], s[64:65], 0, v[130:131]
	v_lshl_add_u64 v[44:45], v[42:43], 0, s[38:39]
	global_load_lds_dwordx4 v[44:45], off
	v_lshl_add_u64 v[42:43], v[42:43], 0, s[40:41]
	s_add_i32 m0, s27, 0xe000
	s_nop 0
	global_load_lds_dwordx4 v[42:43], off
	v_add_u32_e32 v208, s77, v1
	v_mov_b64_e32 v[46:47], v[172:173]
	v_mov_b64_e32 v[50:51], v[176:177]
	v_mov_b64_e32 v[48:49], v[174:175]
	ds_read_b128 v[172:175], v208
	v_mov_b64_e32 v[52:53], v[178:179]
	ds_read_b128 v[176:179], v208 offset:1024
	ds_read_b128 v[180:183], v208 offset:2048
	ds_read_b128 v[184:187], v208 offset:3072
	ds_read_b128 v[196:199], v208 offset:4096
	ds_read_b128 v[200:203], v208 offset:5120
	ds_read_b128 v[204:207], v208 offset:6144
	ds_read_b128 v[208:211], v208 offset:7168
	s_waitcnt vmcnt(8)
	s_waitcnt lgkmcnt(0)
	s_barrier
	s_setprio 1
	s_waitcnt lgkmcnt(0)
	v_mfma_scale_f32_16x16x128_f8f6f4 v[94:97], v[140:147], v[172:179], v[94:97], v138, v138 op_sel_hi:[0,0,0]
	v_mfma_scale_f32_16x16x128_f8f6f4 v[90:93], v[148:155], v[172:179], v[90:93], v138, v138 op_sel_hi:[0,0,0]
	v_mfma_scale_f32_16x16x128_f8f6f4 v[86:89], v[140:147], v[180:187], v[86:89], v138, v138 op_sel_hi:[0,0,0]
	v_mfma_scale_f32_16x16x128_f8f6f4 v[82:85], v[148:155], v[180:187], v[82:85], v138, v138 op_sel_hi:[0,0,0]
	v_mfma_scale_f32_16x16x128_f8f6f4 v[78:81], v[140:147], v[196:203], v[78:81], v138, v138 op_sel_hi:[0,0,0]
	v_mfma_scale_f32_16x16x128_f8f6f4 v[74:77], v[148:155], v[196:203], v[74:77], v138, v138 op_sel_hi:[0,0,0]
	v_mfma_scale_f32_16x16x128_f8f6f4 v[134:137], v[140:147], v[204:211], v[70:73], v138, v138 op_sel_hi:[0,0,0]
	v_mfma_scale_f32_16x16x128_f8f6f4 v[188:191], v[148:155], v[204:211], v[66:69], v138, v138 op_sel_hi:[0,0,0]
	v_mfma_scale_f32_16x16x128_f8f6f4 v[192:195], v[156:163], v[172:179], v[62:65], v138, v138 op_sel_hi:[0,0,0]
	v_mfma_scale_f32_16x16x128_f8f6f4 v[172:175], v[164:171], v[172:179], v[58:61], v138, v138 op_sel_hi:[0,0,0]
	v_mfma_scale_f32_16x16x128_f8f6f4 v[176:179], v[156:163], v[180:187], v[54:57], v138, v138 op_sel_hi:[0,0,0]
	v_mfma_scale_f32_16x16x128_f8f6f4 v[180:183], v[164:171], v[180:187], v[50:53], v138, v138 op_sel_hi:[0,0,0]
	v_mfma_scale_f32_16x16x128_f8f6f4 v[184:187], v[156:163], v[196:203], v[46:49], v138, v138 op_sel_hi:[0,0,0]
	v_mfma_scale_f32_16x16x128_f8f6f4 v[196:199], v[164:171], v[196:203], v[18:21], v138, v138 op_sel_hi:[0,0,0]
	v_mfma_scale_f32_16x16x128_f8f6f4 v[200:203], v[156:163], v[204:211], v[6:9], v138, v138 op_sel_hi:[0,0,0]
	v_mfma_scale_f32_16x16x128_f8f6f4 v[204:207], v[164:171], v[204:211], v[14:17], v138, v138 op_sel_hi:[0,0,0]
	s_setprio 0
	s_barrier
	v_mov_b32_e32 v133, v131
	s_nop 2
	s_add_i32 s34, s79, s3
	s_mov_b32 m0, s34
	v_lshl_add_u64 v[6:7], s[62:63], 0, v[132:133]
	global_load_lds_dwordx4 v132, s[62:63]
	v_lshl_add_u64 v[6:7], v[6:7], 0, s[20:21]
	s_add_i32 m0, s34, 0x2000
	s_add_i32 s34, s81, s3
	global_load_lds_dwordx4 v[6:7], off
	s_mov_b32 m0, s34
	v_lshl_add_u64 v[6:7], s[62:63], 0, v[132:133]
	v_lshl_add_u64 v[8:9], v[6:7], 0, s[22:23]
	global_load_lds_dwordx4 v[8:9], off
	v_lshl_add_u64 v[6:7], v[6:7], 0, s[24:25]
	s_add_i32 m0, s34, 0x2000
	s_nop 0
	global_load_lds_dwordx4 v[6:7], off
	s_mov_b32 m0, s27
	v_lshl_add_u64 v[6:7], s[60:61], 0, v[130:131]
	global_load_lds_dwordx4 v130, s[60:61]
	v_lshl_add_u64 v[6:7], v[6:7], 0, s[20:21]
	s_mov_b32 m0, s70
	s_nop 0
	global_load_lds_dwordx4 v[6:7], off
	v_add_u32_e32 v70, s77, v1
	ds_read_b128 v[42:45], v70 offset:16384
	ds_read_b128 v[46:49], v70 offset:17408
	ds_read_b128 v[50:53], v70 offset:18432
	ds_read_b128 v[54:57], v70 offset:19456
	ds_read_b128 v[58:61], v70 offset:20480
	ds_read_b128 v[62:65], v70 offset:21504
	ds_read_b128 v[66:69], v70 offset:22528
	ds_read_b128 v[70:73], v70 offset:23552
	s_waitcnt vmcnt(8)
	s_waitcnt lgkmcnt(0)
	s_barrier
	s_setprio 1
	s_waitcnt lgkmcnt(0)
	v_mfma_scale_f32_16x16x128_f8f6f4 v[38:41], v[140:147], v[42:49], v[38:41], v138, v138 op_sel_hi:[0,0,0]
	v_mfma_scale_f32_16x16x128_f8f6f4 v[34:37], v[148:155], v[42:49], v[34:37], v138, v138 op_sel_hi:[0,0,0]
	v_mfma_scale_f32_16x16x128_f8f6f4 v[220:223], v[148:155], v[58:65], v[220:223], v138, v138 op_sel_hi:[0,0,0]
	v_mfma_scale_f32_16x16x128_f8f6f4 v[208:211], v[140:147], v[50:57], v[30:33], v138, v138 op_sel_hi:[0,0,0]
	v_mfma_scale_f32_16x16x128_f8f6f4 v[212:215], v[148:155], v[50:57], v[26:29], v138, v138 op_sel_hi:[0,0,0]
	v_mfma_scale_f32_16x16x128_f8f6f4 v[216:219], v[140:147], v[58:65], v[22:25], v138, v138 op_sel_hi:[0,0,0]
	v_mfma_scale_f32_16x16x128_f8f6f4 v[224:227], v[140:147], v[66:73], v[2:5], v138, v138 op_sel_hi:[0,0,0]
	v_mfma_scale_f32_16x16x128_f8f6f4 v[228:231], v[148:155], v[66:73], v[10:13], v138, v138 op_sel_hi:[0,0,0]
	v_mfma_scale_f32_16x16x128_f8f6f4 v[232:235], v[156:163], v[42:49], v[98:101], v138, v138 op_sel_hi:[0,0,0]
	v_mfma_scale_f32_16x16x128_f8f6f4 v[236:239], v[164:171], v[42:49], v[102:105], v138, v138 op_sel_hi:[0,0,0]
	v_mfma_scale_f32_16x16x128_f8f6f4 v[240:243], v[156:163], v[50:57], v[106:109], v138, v138 op_sel_hi:[0,0,0]
	v_mfma_scale_f32_16x16x128_f8f6f4 v[244:247], v[164:171], v[50:57], v[110:113], v138, v138 op_sel_hi:[0,0,0]
	v_mfma_scale_f32_16x16x128_f8f6f4 v[248:251], v[156:163], v[58:65], v[114:117], v138, v138 op_sel_hi:[0,0,0]
	v_mfma_scale_f32_16x16x128_f8f6f4 v[42:45], v[164:171], v[58:65], v[118:121], v138, v138 op_sel_hi:[0,0,0]
	v_mfma_scale_f32_16x16x128_f8f6f4 v[46:49], v[156:163], v[66:73], v[122:125], v138, v138 op_sel_hi:[0,0,0]
	v_mfma_scale_f32_16x16x128_f8f6f4 v[50:53], v[164:171], v[66:73], v[126:129], v138, v138 op_sel_hi:[0,0,0]
	s_setprio 0
	s_barrier
	s_mov_b32 m0, s71
	v_lshl_add_u64 v[54:55], s[60:61], 0, v[130:131]
	v_lshl_add_u64 v[56:57], v[54:55], 0, s[22:23]
	global_load_lds_dwordx4 v[56:57], off
	v_lshl_add_u64 v[54:55], v[54:55], 0, s[24:25]
	s_mov_b32 m0, s72
	s_nop 0
	global_load_lds_dwordx4 v[54:55], off
	s_add_i32 s34, 0, 0x18000
	v_add_u32_e32 v2, s76, v1
	s_add_i32 s35, 0, 0x1c000
	v_add_u32_e32 v110, s34, v2
	v_add_u32_e32 v2, s35, v2
	ds_read_b128 v[98:101], v110
	ds_read_b128 v[102:105], v110 offset:1024
	ds_read_b128 v[106:109], v110 offset:2048
	ds_read_b128 v[110:113], v110 offset:3072
	ds_read_b128 v[122:125], v2
	ds_read_b128 v[126:129], v2 offset:1024
	ds_read_b128 v[140:143], v2 offset:2048
	ds_read_b128 v[144:147], v2 offset:3072
	v_add_u32_e32 v30, s77, v1
	ds_read_b128 v[2:5], v30 offset:32768
	ds_read_b128 v[6:9], v30 offset:33792
	ds_read_b128 v[10:13], v30 offset:34816
	ds_read_b128 v[14:17], v30 offset:35840
	ds_read_b128 v[18:21], v30 offset:36864
	ds_read_b128 v[22:25], v30 offset:37888
	ds_read_b128 v[26:29], v30 offset:38912
	ds_read_b128 v[30:33], v30 offset:39936
	s_waitcnt vmcnt(8)
	s_waitcnt lgkmcnt(0)
	s_barrier
	s_setprio 1
	s_waitcnt lgkmcnt(0)
	v_mfma_scale_f32_16x16x128_f8f6f4 v[94:97], v[98:105], v[2:9], v[94:97], v138, v138 op_sel_hi:[0,0,0]
	v_mfma_scale_f32_16x16x128_f8f6f4 v[90:93], v[106:113], v[2:9], v[90:93], v138, v138 op_sel_hi:[0,0,0]
	v_mfma_scale_f32_16x16x128_f8f6f4 v[86:89], v[98:105], v[10:17], v[86:89], v138, v138 op_sel_hi:[0,0,0]
	v_mfma_scale_f32_16x16x128_f8f6f4 v[82:85], v[106:113], v[10:17], v[82:85], v138, v138 op_sel_hi:[0,0,0]
	v_mfma_scale_f32_16x16x128_f8f6f4 v[78:81], v[98:105], v[18:25], v[78:81], v138, v138 op_sel_hi:[0,0,0]
	v_mfma_scale_f32_16x16x128_f8f6f4 v[74:77], v[106:113], v[18:25], v[74:77], v138, v138 op_sel_hi:[0,0,0]
	v_mfma_scale_f32_16x16x128_f8f6f4 v[70:73], v[98:105], v[26:33], v[134:137], v138, v138 op_sel_hi:[0,0,0]
	v_mfma_scale_f32_16x16x128_f8f6f4 v[66:69], v[106:113], v[26:33], v[188:191], v138, v138 op_sel_hi:[0,0,0]
	v_mfma_scale_f32_16x16x128_f8f6f4 v[62:65], v[122:129], v[2:9], v[192:195], v138, v138 op_sel_hi:[0,0,0]
	v_mfma_scale_f32_16x16x128_f8f6f4 v[58:61], v[140:147], v[2:9], v[172:175], v138, v138 op_sel_hi:[0,0,0]
	v_mfma_scale_f32_16x16x128_f8f6f4 v[54:57], v[122:129], v[10:17], v[176:179], v138, v138 op_sel_hi:[0,0,0]
	v_mfma_scale_f32_16x16x128_f8f6f4 v[176:179], v[140:147], v[10:17], v[180:183], v138, v138 op_sel_hi:[0,0,0]
	v_mfma_scale_f32_16x16x128_f8f6f4 v[172:175], v[122:129], v[18:25], v[184:187], v138, v138 op_sel_hi:[0,0,0]
	v_mfma_scale_f32_16x16x128_f8f6f4 v[18:21], v[140:147], v[18:25], v[196:199], v138, v138 op_sel_hi:[0,0,0]
	v_mfma_scale_f32_16x16x128_f8f6f4 v[6:9], v[122:129], v[26:33], v[200:203], v138, v138 op_sel_hi:[0,0,0]
	v_mfma_scale_f32_16x16x128_f8f6f4 v[14:17], v[140:147], v[26:33], v[204:207], v138, v138 op_sel_hi:[0,0,0]
	s_setprio 0
	s_barrier
	s_add_i32 s34, s34, s3
	s_mov_b32 m0, s34
	v_lshl_add_u64 v[2:3], s[62:63], 0, v[132:133]
	v_lshl_add_u64 v[4:5], v[2:3], 0, s[30:31]
	global_load_lds_dwordx4 v[4:5], off
	v_lshl_add_u64 v[2:3], v[2:3], 0, s[36:37]
	s_add_i32 m0, s34, 0x2000
	s_add_i32 s34, s35, s3
	global_load_lds_dwordx4 v[2:3], off
	s_mov_b32 m0, s34
	v_lshl_add_u64 v[2:3], s[62:63], 0, v[132:133]
	v_lshl_add_u64 v[4:5], v[2:3], 0, s[38:39]
	global_load_lds_dwordx4 v[4:5], off
	v_lshl_add_u64 v[2:3], v[2:3], 0, s[40:41]
	s_add_i32 m0, s34, 0x2000
	s_nop 0
	global_load_lds_dwordx4 v[2:3], off
	s_mov_b32 m0, s73
	v_lshl_add_u64 v[2:3], s[60:61], 0, v[130:131]
	v_lshl_add_u64 v[4:5], v[2:3], 0, s[30:31]
	global_load_lds_dwordx4 v[4:5], off
	v_lshl_add_u64 v[2:3], v[2:3], 0, s[36:37]
	s_mov_b32 m0, s74
	s_nop 0
	global_load_lds_dwordx4 v[2:3], off
	v_add_u32_e32 v168, s77, v1
	ds_read_b128 v[114:117], v168 offset:49152
	ds_read_b128 v[118:121], v168 offset:50176
	ds_read_b128 v[148:151], v168 offset:51200
	ds_read_b128 v[152:155], v168 offset:52224
	ds_read_b128 v[156:159], v168 offset:53248
	ds_read_b128 v[160:163], v168 offset:54272
	ds_read_b128 v[164:167], v168 offset:55296
	ds_read_b128 v[168:171], v168 offset:56320
	s_waitcnt vmcnt(8)
	s_waitcnt lgkmcnt(0)
	s_barrier
	s_setprio 1
	s_waitcnt lgkmcnt(0)
	v_mfma_scale_f32_16x16x128_f8f6f4 v[38:41], v[98:105], v[114:121], v[38:41], v138, v138 op_sel_hi:[0,0,0]
	v_mfma_scale_f32_16x16x128_f8f6f4 v[34:37], v[106:113], v[114:121], v[34:37], v138, v138 op_sel_hi:[0,0,0]
	v_mfma_scale_f32_16x16x128_f8f6f4 v[30:33], v[98:105], v[148:155], v[208:211], v138, v138 op_sel_hi:[0,0,0]
	v_mfma_scale_f32_16x16x128_f8f6f4 v[26:29], v[106:113], v[148:155], v[212:215], v138, v138 op_sel_hi:[0,0,0]
	v_mfma_scale_f32_16x16x128_f8f6f4 v[22:25], v[98:105], v[156:163], v[216:219], v138, v138 op_sel_hi:[0,0,0]
	v_mfma_scale_f32_16x16x128_f8f6f4 v[220:223], v[106:113], v[156:163], v[220:223], v138, v138 op_sel_hi:[0,0,0]
	v_mfma_scale_f32_16x16x128_f8f6f4 v[2:5], v[98:105], v[164:171], v[224:227], v138, v138 op_sel_hi:[0,0,0]
	v_mfma_scale_f32_16x16x128_f8f6f4 v[10:13], v[106:113], v[164:171], v[228:231], v138, v138 op_sel_hi:[0,0,0]
	v_mfma_scale_f32_16x16x128_f8f6f4 v[98:101], v[122:129], v[114:121], v[232:235], v138, v138 op_sel_hi:[0,0,0]
	v_mfma_scale_f32_16x16x128_f8f6f4 v[102:105], v[140:147], v[114:121], v[236:239], v138, v138 op_sel_hi:[0,0,0]
	v_mfma_scale_f32_16x16x128_f8f6f4 v[106:109], v[122:129], v[148:155], v[240:243], v138, v138 op_sel_hi:[0,0,0]
	v_mfma_scale_f32_16x16x128_f8f6f4 v[110:113], v[140:147], v[148:155], v[244:247], v138, v138 op_sel_hi:[0,0,0]
	v_mfma_scale_f32_16x16x128_f8f6f4 v[114:117], v[122:129], v[156:163], v[248:251], v138, v138 op_sel_hi:[0,0,0]
	v_mfma_scale_f32_16x16x128_f8f6f4 v[118:121], v[140:147], v[156:163], v[42:45], v138, v138 op_sel_hi:[0,0,0]
	v_mfma_scale_f32_16x16x128_f8f6f4 v[122:125], v[122:129], v[164:171], v[46:49], v138, v138 op_sel_hi:[0,0,0]
	v_mfma_scale_f32_16x16x128_f8f6f4 v[126:129], v[140:147], v[164:171], v[50:53], v138, v138 op_sel_hi:[0,0,0]
	s_setprio 0
	s_barrier
	s_add_i32 s51, s51, 2
	s_add_u32 s58, s58, 0x100
	s_addc_u32 s59, s59, 0
	s_cmp_gt_u32 s51, 13
	s_cbranch_scc0 .LBB0_1224
	s_and_b64 vcc, exec, s[44:45]
	s_cbranch_vccz .LBB0_1227
	s_barrier

.LBB0_1257:
	s_add_u32 s60, s42, s54
	v_add_u32_e32 v42, s75, v1
	v_add_u32_e32 v152, s78, v42
	v_add_u32_e32 v42, s79, v42
	ds_read_b128 v[140:143], v152
	ds_read_b128 v[144:147], v152 offset:1024
	ds_read_b128 v[148:151], v152 offset:2048
	ds_read_b128 v[152:155], v152 offset:3072
	ds_read_b128 v[156:159], v42
	ds_read_b128 v[160:163], v42 offset:1024
	ds_read_b128 v[164:167], v42 offset:2048
	ds_read_b128 v[168:171], v42 offset:3072
	s_addc_u32 s61, s43, s55
	s_add_u32 s34, s60, 0x100
	s_addc_u32 s35, s61, 0
	s_add_u32 s58, s45, s54
	s_addc_u32 s59, s47, s55
	s_cmpk_eq_i32 s54, 0x700
	s_cselect_b32 s57, s51, s35
	s_cselect_b32 s56, s50, s34
	s_cselect_b32 s59, s53, s59
	s_cselect_b32 s58, s52, s58
	s_add_i32 m0, s23, 0xc000
	v_lshl_add_u64 v[42:43], s[60:61], 0, v[130:131]
	v_lshl_add_u64 v[44:45], v[42:43], 0, s[30:31]
	global_load_lds_dwordx4 v[44:45], off
	v_lshl_add_u64 v[42:43], v[42:43], 0, s[36:37]
	s_add_i32 m0, s23, 0xe000
	s_nop 0
	global_load_lds_dwordx4 v[42:43], off
	v_add_u32_e32 v208, s76, v1
	v_mov_b64_e32 v[46:47], v[172:173]
	v_mov_b64_e32 v[50:51], v[176:177]
	v_mov_b64_e32 v[48:49], v[174:175]
	ds_read_b128 v[172:175], v208
	v_mov_b64_e32 v[52:53], v[178:179]
	ds_read_b128 v[176:179], v208 offset:1024
	ds_read_b128 v[180:183], v208 offset:2048
	ds_read_b128 v[184:187], v208 offset:3072
	ds_read_b128 v[196:199], v208 offset:4096
	ds_read_b128 v[200:203], v208 offset:5120
	ds_read_b128 v[204:207], v208 offset:6144
	ds_read_b128 v[208:211], v208 offset:7168
	s_waitcnt vmcnt(8)
	s_waitcnt lgkmcnt(0)
	s_barrier
	s_setprio 1
	s_waitcnt lgkmcnt(0)
	v_mfma_scale_f32_16x16x128_f8f6f4 v[94:97], v[140:147], v[172:179], v[94:97], v138, v138 op_sel_hi:[0,0,0]
	v_mfma_scale_f32_16x16x128_f8f6f4 v[90:93], v[148:155], v[172:179], v[90:93], v138, v138 op_sel_hi:[0,0,0]
	v_mfma_scale_f32_16x16x128_f8f6f4 v[86:89], v[140:147], v[180:187], v[86:89], v138, v138 op_sel_hi:[0,0,0]
	v_mfma_scale_f32_16x16x128_f8f6f4 v[82:85], v[148:155], v[180:187], v[82:85], v138, v138 op_sel_hi:[0,0,0]
	v_mfma_scale_f32_16x16x128_f8f6f4 v[78:81], v[140:147], v[196:203], v[78:81], v138, v138 op_sel_hi:[0,0,0]
	v_mfma_scale_f32_16x16x128_f8f6f4 v[74:77], v[148:155], v[196:203], v[74:77], v138, v138 op_sel_hi:[0,0,0]
	v_mfma_scale_f32_16x16x128_f8f6f4 v[134:137], v[140:147], v[204:211], v[70:73], v138, v138 op_sel_hi:[0,0,0]
	v_mfma_scale_f32_16x16x128_f8f6f4 v[188:191], v[148:155], v[204:211], v[66:69], v138, v138 op_sel_hi:[0,0,0]
	v_mfma_scale_f32_16x16x128_f8f6f4 v[192:195], v[156:163], v[172:179], v[62:65], v138, v138 op_sel_hi:[0,0,0]
	v_mfma_scale_f32_16x16x128_f8f6f4 v[172:175], v[164:171], v[172:179], v[58:61], v138, v138 op_sel_hi:[0,0,0]
	v_mfma_scale_f32_16x16x128_f8f6f4 v[176:179], v[156:163], v[180:187], v[54:57], v138, v138 op_sel_hi:[0,0,0]
	v_mfma_scale_f32_16x16x128_f8f6f4 v[180:183], v[164:171], v[180:187], v[50:53], v138, v138 op_sel_hi:[0,0,0]
	v_mfma_scale_f32_16x16x128_f8f6f4 v[184:187], v[156:163], v[196:203], v[46:49], v138, v138 op_sel_hi:[0,0,0]
	v_mfma_scale_f32_16x16x128_f8f6f4 v[196:199], v[164:171], v[196:203], v[18:21], v138, v138 op_sel_hi:[0,0,0]
	v_mfma_scale_f32_16x16x128_f8f6f4 v[200:203], v[156:163], v[204:211], v[6:9], v138, v138 op_sel_hi:[0,0,0]
	v_mfma_scale_f32_16x16x128_f8f6f4 v[204:207], v[164:171], v[204:211], v[14:17], v138, v138 op_sel_hi:[0,0,0]
	s_setprio 0
	s_barrier
	v_mov_b32_e32 v133, v131
	s_nop 2
	s_add_i32 s34, s78, s39
	s_mov_b32 m0, s34
	v_lshl_add_u64 v[6:7], s[58:59], 0, v[132:133]
	global_load_lds_dwordx4 v132, s[58:59]
	v_lshl_add_u64 v[6:7], v[6:7], 0, s[8:9]
	s_add_i32 m0, s34, 0x2000
	s_add_i32 s34, s79, s39
	global_load_lds_dwordx4 v[6:7], off
	s_mov_b32 m0, s34
	v_lshl_add_u64 v[6:7], s[58:59], 0, v[132:133]
	v_lshl_add_u64 v[8:9], v[6:7], 0, s[18:19]
	global_load_lds_dwordx4 v[8:9], off
	v_lshl_add_u64 v[6:7], v[6:7], 0, s[20:21]
	s_add_i32 m0, s34, 0x2000
	s_nop 0
	global_load_lds_dwordx4 v[6:7], off
	s_mov_b32 m0, s23
	v_lshl_add_u64 v[6:7], s[56:57], 0, v[130:131]
	global_load_lds_dwordx4 v130, s[56:57]
	v_lshl_add_u64 v[6:7], v[6:7], 0, s[8:9]
	s_mov_b32 m0, s69
	s_nop 0
	global_load_lds_dwordx4 v[6:7], off
	v_add_u32_e32 v70, s76, v1
	ds_read_b128 v[42:45], v70 offset:16384
	ds_read_b128 v[46:49], v70 offset:17408
	ds_read_b128 v[50:53], v70 offset:18432
	ds_read_b128 v[54:57], v70 offset:19456
	ds_read_b128 v[58:61], v70 offset:20480
	ds_read_b128 v[62:65], v70 offset:21504
	ds_read_b128 v[66:69], v70 offset:22528
	ds_read_b128 v[70:73], v70 offset:23552
	s_waitcnt vmcnt(8)
	s_waitcnt lgkmcnt(0)
	s_barrier
	s_setprio 1
	s_waitcnt lgkmcnt(0)
	v_mfma_scale_f32_16x16x128_f8f6f4 v[38:41], v[140:147], v[42:49], v[38:41], v138, v138 op_sel_hi:[0,0,0]
	v_mfma_scale_f32_16x16x128_f8f6f4 v[34:37], v[148:155], v[42:49], v[34:37], v138, v138 op_sel_hi:[0,0,0]
	v_mfma_scale_f32_16x16x128_f8f6f4 v[220:223], v[148:155], v[58:65], v[220:223], v138, v138 op_sel_hi:[0,0,0]
	v_mfma_scale_f32_16x16x128_f8f6f4 v[208:211], v[140:147], v[50:57], v[30:33], v138, v138 op_sel_hi:[0,0,0]
	v_mfma_scale_f32_16x16x128_f8f6f4 v[212:215], v[148:155], v[50:57], v[26:29], v138, v138 op_sel_hi:[0,0,0]
	v_mfma_scale_f32_16x16x128_f8f6f4 v[216:219], v[140:147], v[58:65], v[22:25], v138, v138 op_sel_hi:[0,0,0]
	v_mfma_scale_f32_16x16x128_f8f6f4 v[224:227], v[140:147], v[66:73], v[2:5], v138, v138 op_sel_hi:[0,0,0]
	v_mfma_scale_f32_16x16x128_f8f6f4 v[228:231], v[148:155], v[66:73], v[10:13], v138, v138 op_sel_hi:[0,0,0]
	v_mfma_scale_f32_16x16x128_f8f6f4 v[232:235], v[156:163], v[42:49], v[98:101], v138, v138 op_sel_hi:[0,0,0]
	v_mfma_scale_f32_16x16x128_f8f6f4 v[236:239], v[164:171], v[42:49], v[102:105], v138, v138 op_sel_hi:[0,0,0]
	v_mfma_scale_f32_16x16x128_f8f6f4 v[240:243], v[156:163], v[50:57], v[106:109], v138, v138 op_sel_hi:[0,0,0]
	v_mfma_scale_f32_16x16x128_f8f6f4 v[244:247], v[164:171], v[50:57], v[110:113], v138, v138 op_sel_hi:[0,0,0]
	v_mfma_scale_f32_16x16x128_f8f6f4 v[248:251], v[156:163], v[58:65], v[114:117], v138, v138 op_sel_hi:[0,0,0]
	v_mfma_scale_f32_16x16x128_f8f6f4 v[42:45], v[164:171], v[58:65], v[118:121], v138, v138 op_sel_hi:[0,0,0]
	v_mfma_scale_f32_16x16x128_f8f6f4 v[46:49], v[156:163], v[66:73], v[122:125], v138, v138 op_sel_hi:[0,0,0]
	v_mfma_scale_f32_16x16x128_f8f6f4 v[50:53], v[164:171], v[66:73], v[126:129], v138, v138 op_sel_hi:[0,0,0]
	s_setprio 0
	s_barrier
	s_mov_b32 m0, s70
	v_lshl_add_u64 v[54:55], s[56:57], 0, v[130:131]
	v_lshl_add_u64 v[56:57], v[54:55], 0, s[18:19]
	global_load_lds_dwordx4 v[56:57], off
	v_lshl_add_u64 v[54:55], v[54:55], 0, s[20:21]
	s_mov_b32 m0, s71
	s_nop 0
	global_load_lds_dwordx4 v[54:55], off
	s_add_i32 s34, 0, 0x18000
	v_add_u32_e32 v2, s75, v1
	s_add_i32 s35, 0, 0x1c000
	v_add_u32_e32 v110, s34, v2
	v_add_u32_e32 v2, s35, v2
	ds_read_b128 v[98:101], v110
	ds_read_b128 v[102:105], v110 offset:1024
	ds_read_b128 v[106:109], v110 offset:2048
	ds_read_b128 v[110:113], v110 offset:3072
	ds_read_b128 v[122:125], v2
	ds_read_b128 v[126:129], v2 offset:1024
	ds_read_b128 v[140:143], v2 offset:2048
	ds_read_b128 v[144:147], v2 offset:3072
	v_add_u32_e32 v30, s76, v1
	ds_read_b128 v[2:5], v30 offset:32768
	ds_read_b128 v[6:9], v30 offset:33792
	ds_read_b128 v[10:13], v30 offset:34816
	ds_read_b128 v[14:17], v30 offset:35840
	ds_read_b128 v[18:21], v30 offset:36864
	ds_read_b128 v[22:25], v30 offset:37888
	ds_read_b128 v[26:29], v30 offset:38912
	ds_read_b128 v[30:33], v30 offset:39936
	s_waitcnt vmcnt(8)
	s_waitcnt lgkmcnt(0)
	s_barrier
	s_setprio 1
	s_waitcnt lgkmcnt(0)
	v_mfma_scale_f32_16x16x128_f8f6f4 v[94:97], v[98:105], v[2:9], v[94:97], v138, v138 op_sel_hi:[0,0,0]
	v_mfma_scale_f32_16x16x128_f8f6f4 v[90:93], v[106:113], v[2:9], v[90:93], v138, v138 op_sel_hi:[0,0,0]
	v_mfma_scale_f32_16x16x128_f8f6f4 v[86:89], v[98:105], v[10:17], v[86:89], v138, v138 op_sel_hi:[0,0,0]
	v_mfma_scale_f32_16x16x128_f8f6f4 v[82:85], v[106:113], v[10:17], v[82:85], v138, v138 op_sel_hi:[0,0,0]
	v_mfma_scale_f32_16x16x128_f8f6f4 v[78:81], v[98:105], v[18:25], v[78:81], v138, v138 op_sel_hi:[0,0,0]
	v_mfma_scale_f32_16x16x128_f8f6f4 v[74:77], v[106:113], v[18:25], v[74:77], v138, v138 op_sel_hi:[0,0,0]
	v_mfma_scale_f32_16x16x128_f8f6f4 v[70:73], v[98:105], v[26:33], v[134:137], v138, v138 op_sel_hi:[0,0,0]
	v_mfma_scale_f32_16x16x128_f8f6f4 v[66:69], v[106:113], v[26:33], v[188:191], v138, v138 op_sel_hi:[0,0,0]
	v_mfma_scale_f32_16x16x128_f8f6f4 v[62:65], v[122:129], v[2:9], v[192:195], v138, v138 op_sel_hi:[0,0,0]
	v_mfma_scale_f32_16x16x128_f8f6f4 v[58:61], v[140:147], v[2:9], v[172:175], v138, v138 op_sel_hi:[0,0,0]
	v_mfma_scale_f32_16x16x128_f8f6f4 v[54:57], v[122:129], v[10:17], v[176:179], v138, v138 op_sel_hi:[0,0,0]
	v_mfma_scale_f32_16x16x128_f8f6f4 v[176:179], v[140:147], v[10:17], v[180:183], v138, v138 op_sel_hi:[0,0,0]
	v_mfma_scale_f32_16x16x128_f8f6f4 v[172:175], v[122:129], v[18:25], v[184:187], v138, v138 op_sel_hi:[0,0,0]
	v_mfma_scale_f32_16x16x128_f8f6f4 v[18:21], v[140:147], v[18:25], v[196:199], v138, v138 op_sel_hi:[0,0,0]
	v_mfma_scale_f32_16x16x128_f8f6f4 v[6:9], v[122:129], v[26:33], v[200:203], v138, v138 op_sel_hi:[0,0,0]
	v_mfma_scale_f32_16x16x128_f8f6f4 v[14:17], v[140:147], v[26:33], v[204:207], v138, v138 op_sel_hi:[0,0,0]
	s_setprio 0
	s_barrier
	s_add_i32 s34, s34, s39
	s_mov_b32 m0, s34
	v_lshl_add_u64 v[2:3], s[58:59], 0, v[132:133]
	v_lshl_add_u64 v[4:5], v[2:3], 0, s[26:27]
	global_load_lds_dwordx4 v[4:5], off
	v_lshl_add_u64 v[2:3], v[2:3], 0, s[28:29]
	s_add_i32 m0, s34, 0x2000
	s_add_i32 s34, s35, s39
	global_load_lds_dwordx4 v[2:3], off
	s_mov_b32 m0, s34
	v_lshl_add_u64 v[2:3], s[58:59], 0, v[132:133]
	v_lshl_add_u64 v[4:5], v[2:3], 0, s[30:31]
	global_load_lds_dwordx4 v[4:5], off
	v_lshl_add_u64 v[2:3], v[2:3], 0, s[36:37]
	s_add_i32 m0, s34, 0x2000
	s_nop 0
	global_load_lds_dwordx4 v[2:3], off
	s_mov_b32 m0, s72
	v_lshl_add_u64 v[2:3], s[56:57], 0, v[130:131]
	v_lshl_add_u64 v[4:5], v[2:3], 0, s[26:27]
	global_load_lds_dwordx4 v[4:5], off
	v_lshl_add_u64 v[2:3], v[2:3], 0, s[28:29]
	s_mov_b32 m0, s73
	s_nop 0
	global_load_lds_dwordx4 v[2:3], off
	v_add_u32_e32 v168, s76, v1
	ds_read_b128 v[114:117], v168 offset:49152
	ds_read_b128 v[118:121], v168 offset:50176
	ds_read_b128 v[148:151], v168 offset:51200
	ds_read_b128 v[152:155], v168 offset:52224
	ds_read_b128 v[156:159], v168 offset:53248
	ds_read_b128 v[160:163], v168 offset:54272
	ds_read_b128 v[164:167], v168 offset:55296
	ds_read_b128 v[168:171], v168 offset:56320
	s_waitcnt vmcnt(8)
	s_waitcnt lgkmcnt(0)
	s_barrier
	s_setprio 1
	s_waitcnt lgkmcnt(0)
	v_mfma_scale_f32_16x16x128_f8f6f4 v[38:41], v[98:105], v[114:121], v[38:41], v138, v138 op_sel_hi:[0,0,0]
	v_mfma_scale_f32_16x16x128_f8f6f4 v[34:37], v[106:113], v[114:121], v[34:37], v138, v138 op_sel_hi:[0,0,0]
	v_mfma_scale_f32_16x16x128_f8f6f4 v[30:33], v[98:105], v[148:155], v[208:211], v138, v138 op_sel_hi:[0,0,0]
	v_mfma_scale_f32_16x16x128_f8f6f4 v[26:29], v[106:113], v[148:155], v[212:215], v138, v138 op_sel_hi:[0,0,0]
	v_mfma_scale_f32_16x16x128_f8f6f4 v[22:25], v[98:105], v[156:163], v[216:219], v138, v138 op_sel_hi:[0,0,0]
	v_mfma_scale_f32_16x16x128_f8f6f4 v[220:223], v[106:113], v[156:163], v[220:223], v138, v138 op_sel_hi:[0,0,0]
	v_mfma_scale_f32_16x16x128_f8f6f4 v[2:5], v[98:105], v[164:171], v[224:227], v138, v138 op_sel_hi:[0,0,0]
	v_mfma_scale_f32_16x16x128_f8f6f4 v[10:13], v[106:113], v[164:171], v[228:231], v138, v138 op_sel_hi:[0,0,0]
	v_mfma_scale_f32_16x16x128_f8f6f4 v[98:101], v[122:129], v[114:121], v[232:235], v138, v138 op_sel_hi:[0,0,0]
	v_mfma_scale_f32_16x16x128_f8f6f4 v[102:105], v[140:147], v[114:121], v[236:239], v138, v138 op_sel_hi:[0,0,0]
	v_mfma_scale_f32_16x16x128_f8f6f4 v[106:109], v[122:129], v[148:155], v[240:243], v138, v138 op_sel_hi:[0,0,0]
	v_mfma_scale_f32_16x16x128_f8f6f4 v[110:113], v[140:147], v[148:155], v[244:247], v138, v138 op_sel_hi:[0,0,0]
	v_mfma_scale_f32_16x16x128_f8f6f4 v[114:117], v[122:129], v[156:163], v[248:251], v138, v138 op_sel_hi:[0,0,0]
	v_mfma_scale_f32_16x16x128_f8f6f4 v[118:121], v[140:147], v[156:163], v[42:45], v138, v138 op_sel_hi:[0,0,0]
	v_mfma_scale_f32_16x16x128_f8f6f4 v[122:125], v[122:129], v[164:171], v[46:49], v138, v138 op_sel_hi:[0,0,0]
	v_mfma_scale_f32_16x16x128_f8f6f4 v[126:129], v[140:147], v[164:171], v[50:53], v138, v138 op_sel_hi:[0,0,0]
	s_setprio 0
	s_barrier
	s_add_i32 s86, s86, 2
	s_add_u32 s54, s54, 0x100
	s_addc_u32 s55, s55, 0
	s_cmp_gt_u32 s86, 13
	s_cbranch_scc0 .LBB0_1257
	s_and_b64 vcc, exec, s[40:41]
	s_cbranch_vccz .LBB0_1260
	s_barrier

.LBB0_1308:
	s_add_u32 s34, s4, 0xfffa0080
	s_addc_u32 s35, s5, -1
	s_cmp_eq_u32 s83, 12
	s_cselect_b32 s53, s45, s35
	s_cselect_b32 s52, s44, s34
	s_cselect_b32 s55, s47, s43
	s_cselect_b32 s54, s46, s41
	s_mov_b32 s34, 0xfffe0000
	s_mov_b32 s35, -1
	v_lshl_add_u64 v[192:193], s[4:5], 0, v[130:131]
	v_lshl_add_u64 v[192:193], v[192:193], 0, s[34:35]
	s_add_i32 m0, s51, 0xc000
	s_nop 0
	global_load_lds_dwordx4 v[192:193], off
	s_add_i32 m0, s51, 0xe000
	s_nop 0
	global_load_lds_dwordx4 v130, s[4:5]
	v_add_u32_e32 v133, s71, v1
	v_add_u32_e32 v148, s74, v133
	v_add_u32_e32 v133, s75, v133
	ds_read_b128 v[136:139], v148
	ds_read_b128 v[140:143], v148 offset:1024
	ds_read_b128 v[144:147], v148 offset:2048
	ds_read_b128 v[148:151], v148 offset:3072
	ds_read_b128 v[152:155], v133
	ds_read_b128 v[156:159], v133 offset:1024
	ds_read_b128 v[160:163], v133 offset:2048
	ds_read_b128 v[164:167], v133 offset:3072
	v_add_u32_e32 v133, s72, v1
	ds_read_b128 v[168:171], v133
	ds_read_b128 v[172:175], v133 offset:1024
	ds_read_b128 v[176:179], v133 offset:2048
	ds_read_b128 v[180:183], v133 offset:3072
	ds_read_b128 v[184:187], v133 offset:4096
	ds_read_b128 v[188:191], v133 offset:5120
	ds_read_b128 v[196:199], v133 offset:6144
	ds_read_b128 v[200:203], v133 offset:7168
	s_waitcnt vmcnt(8)
	s_waitcnt lgkmcnt(0)
	s_barrier
	s_setprio 1
	s_waitcnt lgkmcnt(0)
	v_mfma_scale_f32_16x16x128_f8f6f4 v[126:129], v[136:143], v[168:175], v[126:129], v134, v134 op_sel_hi:[0,0,0]
	v_mfma_scale_f32_16x16x128_f8f6f4 v[122:125], v[144:151], v[168:175], v[122:125], v134, v134 op_sel_hi:[0,0,0]
	v_mfma_scale_f32_16x16x128_f8f6f4 v[110:113], v[136:143], v[176:183], v[110:113], v134, v134 op_sel_hi:[0,0,0]
	v_mfma_scale_f32_16x16x128_f8f6f4 v[106:109], v[144:151], v[176:183], v[106:109], v134, v134 op_sel_hi:[0,0,0]
	v_mfma_scale_f32_16x16x128_f8f6f4 v[192:195], v[136:143], v[184:191], v[94:97], v134, v134 op_sel_hi:[0,0,0]
	v_mfma_scale_f32_16x16x128_f8f6f4 v[204:207], v[144:151], v[184:191], v[90:93], v134, v134 op_sel_hi:[0,0,0]
	v_mfma_scale_f32_16x16x128_f8f6f4 v[208:211], v[136:143], v[196:203], v[78:81], v134, v134 op_sel_hi:[0,0,0]
	v_mfma_scale_f32_16x16x128_f8f6f4 v[212:215], v[144:151], v[196:203], v[74:77], v134, v134 op_sel_hi:[0,0,0]
	v_mfma_scale_f32_16x16x128_f8f6f4 v[118:121], v[152:159], v[168:175], v[118:121], v134, v134 op_sel_hi:[0,0,0]
	v_mfma_scale_f32_16x16x128_f8f6f4 v[114:117], v[160:167], v[168:175], v[114:117], v134, v134 op_sel_hi:[0,0,0]
	v_mfma_scale_f32_16x16x128_f8f6f4 v[102:105], v[152:159], v[176:183], v[102:105], v134, v134 op_sel_hi:[0,0,0]
	v_mfma_scale_f32_16x16x128_f8f6f4 v[98:101], v[160:167], v[176:183], v[98:101], v134, v134 op_sel_hi:[0,0,0]
	v_mfma_scale_f32_16x16x128_f8f6f4 v[168:171], v[152:159], v[184:191], v[86:89], v134, v134 op_sel_hi:[0,0,0]
	v_mfma_scale_f32_16x16x128_f8f6f4 v[172:175], v[160:167], v[184:191], v[82:85], v134, v134 op_sel_hi:[0,0,0]
	v_mfma_scale_f32_16x16x128_f8f6f4 v[176:179], v[152:159], v[196:203], v[66:69], v134, v134 op_sel_hi:[0,0,0]
	v_mfma_scale_f32_16x16x128_f8f6f4 v[180:183], v[160:167], v[196:203], v[70:73], v134, v134 op_sel_hi:[0,0,0]
	s_setprio 0
	s_barrier
	v_mov_b32_e32 v133, v131
	s_add_i32 s34, s74, s62
	s_mov_b32 m0, s34
	v_lshl_add_u64 v[184:185], s[54:55], 0, v[132:133]
	global_load_lds_dwordx4 v132, s[54:55]
	v_lshl_add_u64 v[184:185], v[184:185], 0, s[8:9]
	s_add_i32 m0, s34, 0x2000
	s_add_i32 s34, s75, s62
	global_load_lds_dwordx4 v[184:185], off
	s_mov_b32 m0, s34
	v_lshl_add_u64 v[184:185], s[54:55], 0, v[132:133]
	v_lshl_add_u64 v[186:187], v[184:185], 0, s[12:13]
	global_load_lds_dwordx4 v[186:187], off
	v_lshl_add_u64 v[184:185], v[184:185], 0, s[14:15]
	s_add_i32 m0, s34, 0x2000
	s_nop 0
	global_load_lds_dwordx4 v[184:185], off
	s_mov_b32 m0, s51
	v_lshl_add_u64 v[184:185], s[52:53], 0, v[130:131]
	global_load_lds_dwordx4 v130, s[52:53]
	v_lshl_add_u64 v[184:185], v[184:185], 0, s[8:9]
	s_mov_b32 m0, s64
	s_nop 0
	global_load_lds_dwordx4 v[184:185], off
	v_add_u32_e32 v94, s72, v1
	ds_read_b128 v[66:69], v94 offset:16384
	ds_read_b128 v[70:73], v94 offset:17408
	ds_read_b128 v[74:77], v94 offset:18432
	ds_read_b128 v[78:81], v94 offset:19456
	ds_read_b128 v[82:85], v94 offset:20480
	ds_read_b128 v[86:89], v94 offset:21504
	ds_read_b128 v[90:93], v94 offset:22528
	ds_read_b128 v[94:97], v94 offset:23552
	s_waitcnt vmcnt(8)
	s_waitcnt lgkmcnt(0)
	s_barrier
	s_setprio 1
	s_waitcnt lgkmcnt(0)
	v_mfma_scale_f32_16x16x128_f8f6f4 v[62:65], v[136:143], v[66:73], v[62:65], v134, v134 op_sel_hi:[0,0,0]
	v_mfma_scale_f32_16x16x128_f8f6f4 v[58:61], v[144:151], v[66:73], v[58:61], v134, v134 op_sel_hi:[0,0,0]
	v_mfma_scale_f32_16x16x128_f8f6f4 v[10:13], v[136:143], v[90:97], v[10:13], v134, v134 op_sel_hi:[0,0,0]
	v_mfma_scale_f32_16x16x128_f8f6f4 v[184:187], v[136:143], v[74:81], v[46:49], v134, v134 op_sel_hi:[0,0,0]
	v_mfma_scale_f32_16x16x128_f8f6f4 v[188:191], v[144:151], v[74:81], v[42:45], v134, v134 op_sel_hi:[0,0,0]
	v_mfma_scale_f32_16x16x128_f8f6f4 v[196:199], v[136:143], v[82:89], v[30:33], v134, v134 op_sel_hi:[0,0,0]
	v_mfma_scale_f32_16x16x128_f8f6f4 v[200:203], v[144:151], v[82:89], v[26:29], v134, v134 op_sel_hi:[0,0,0]
	v_mfma_scale_f32_16x16x128_f8f6f4 v[216:219], v[144:151], v[90:97], v[14:17], v134, v134 op_sel_hi:[0,0,0]
	v_mfma_scale_f32_16x16x128_f8f6f4 v[54:57], v[152:159], v[66:73], v[54:57], v134, v134 op_sel_hi:[0,0,0]
	v_mfma_scale_f32_16x16x128_f8f6f4 v[220:223], v[160:167], v[66:73], v[50:53], v134, v134 op_sel_hi:[0,0,0]
	v_mfma_scale_f32_16x16x128_f8f6f4 v[224:227], v[152:159], v[74:81], v[38:41], v134, v134 op_sel_hi:[0,0,0]
	v_mfma_scale_f32_16x16x128_f8f6f4 v[228:231], v[160:167], v[74:81], v[34:37], v134, v134 op_sel_hi:[0,0,0]
	v_mfma_scale_f32_16x16x128_f8f6f4 v[232:235], v[152:159], v[82:89], v[22:25], v134, v134 op_sel_hi:[0,0,0]
	v_mfma_scale_f32_16x16x128_f8f6f4 v[236:239], v[160:167], v[82:89], v[18:21], v134, v134 op_sel_hi:[0,0,0]
	v_mfma_scale_f32_16x16x128_f8f6f4 v[240:243], v[152:159], v[90:97], v[6:9], v134, v134 op_sel_hi:[0,0,0]
	v_mfma_scale_f32_16x16x128_f8f6f4 v[244:247], v[160:167], v[90:97], v[2:5], v134, v134 op_sel_hi:[0,0,0]
	s_setprio 0
	s_barrier
	s_mov_b32 m0, s65
	v_lshl_add_u64 v[66:67], s[52:53], 0, v[130:131]
	v_lshl_add_u64 v[68:69], v[66:67], 0, s[12:13]
	global_load_lds_dwordx4 v[68:69], off
	v_lshl_add_u64 v[66:67], v[66:67], 0, s[14:15]
	s_mov_b32 m0, s66
	s_nop 0
	global_load_lds_dwordx4 v[66:67], off
	s_add_i32 s34, 0, 0x18000
	v_add_u32_e32 v22, s71, v1
	s_add_i32 s35, 0, 0x1c000
	v_add_u32_e32 v18, s34, v22
	v_add_u32_e32 v22, s35, v22
	ds_read_b128 v[2:5], v18
	ds_read_b128 v[6:9], v18 offset:1024
	ds_read_b128 v[14:17], v18 offset:2048
	ds_read_b128 v[18:21], v18 offset:3072
	ds_read_b128 v[136:139], v22
	ds_read_b128 v[140:143], v22 offset:1024
	ds_read_b128 v[144:147], v22 offset:2048
	ds_read_b128 v[148:151], v22 offset:3072
	v_add_u32_e32 v50, s72, v1
	ds_read_b128 v[22:25], v50 offset:32768
	ds_read_b128 v[26:29], v50 offset:33792
	ds_read_b128 v[30:33], v50 offset:34816
	ds_read_b128 v[34:37], v50 offset:35840
	ds_read_b128 v[38:41], v50 offset:36864
	ds_read_b128 v[42:45], v50 offset:37888
	ds_read_b128 v[46:49], v50 offset:38912
	ds_read_b128 v[50:53], v50 offset:39936
	s_waitcnt vmcnt(8)
	s_waitcnt lgkmcnt(0)
	s_barrier
	s_setprio 1
	s_waitcnt lgkmcnt(0)
	v_mfma_scale_f32_16x16x128_f8f6f4 v[126:129], v[2:9], v[22:29], v[126:129], v134, v134 op_sel_hi:[0,0,0]
	v_mfma_scale_f32_16x16x128_f8f6f4 v[122:125], v[14:21], v[22:29], v[122:125], v134, v134 op_sel_hi:[0,0,0]
	v_mfma_scale_f32_16x16x128_f8f6f4 v[110:113], v[2:9], v[30:37], v[110:113], v134, v134 op_sel_hi:[0,0,0]
	v_mfma_scale_f32_16x16x128_f8f6f4 v[106:109], v[14:21], v[30:37], v[106:109], v134, v134 op_sel_hi:[0,0,0]
	v_mfma_scale_f32_16x16x128_f8f6f4 v[94:97], v[2:9], v[38:45], v[192:195], v134, v134 op_sel_hi:[0,0,0]
	v_mfma_scale_f32_16x16x128_f8f6f4 v[90:93], v[14:21], v[38:45], v[204:207], v134, v134 op_sel_hi:[0,0,0]
	v_mfma_scale_f32_16x16x128_f8f6f4 v[78:81], v[2:9], v[46:53], v[208:211], v134, v134 op_sel_hi:[0,0,0]
	v_mfma_scale_f32_16x16x128_f8f6f4 v[74:77], v[14:21], v[46:53], v[212:215], v134, v134 op_sel_hi:[0,0,0]
	v_mfma_scale_f32_16x16x128_f8f6f4 v[118:121], v[136:143], v[22:29], v[118:121], v134, v134 op_sel_hi:[0,0,0]
	v_mfma_scale_f32_16x16x128_f8f6f4 v[114:117], v[144:151], v[22:29], v[114:117], v134, v134 op_sel_hi:[0,0,0]
	v_mfma_scale_f32_16x16x128_f8f6f4 v[102:105], v[136:143], v[30:37], v[102:105], v134, v134 op_sel_hi:[0,0,0]
	v_mfma_scale_f32_16x16x128_f8f6f4 v[98:101], v[144:151], v[30:37], v[98:101], v134, v134 op_sel_hi:[0,0,0]
	v_mfma_scale_f32_16x16x128_f8f6f4 v[86:89], v[136:143], v[38:45], v[168:171], v134, v134 op_sel_hi:[0,0,0]
	v_mfma_scale_f32_16x16x128_f8f6f4 v[82:85], v[144:151], v[38:45], v[172:175], v134, v134 op_sel_hi:[0,0,0]
	v_mfma_scale_f32_16x16x128_f8f6f4 v[66:69], v[136:143], v[46:53], v[176:179], v134, v134 op_sel_hi:[0,0,0]
	v_mfma_scale_f32_16x16x128_f8f6f4 v[70:73], v[144:151], v[46:53], v[180:183], v134, v134 op_sel_hi:[0,0,0]
	s_setprio 0
	s_barrier
	s_add_i32 s34, s34, s62
	s_mov_b32 m0, s34
	v_lshl_add_u64 v[22:23], s[54:55], 0, v[132:133]
	v_lshl_add_u64 v[24:25], v[22:23], 0, s[20:21]
	global_load_lds_dwordx4 v[24:25], off
	v_lshl_add_u64 v[22:23], v[22:23], 0, s[22:23]
	s_add_i32 m0, s34, 0x2000
	s_add_i32 s34, s35, s62
	global_load_lds_dwordx4 v[22:23], off
	s_mov_b32 m0, s34
	v_lshl_add_u64 v[22:23], s[54:55], 0, v[132:133]
	v_lshl_add_u64 v[24:25], v[22:23], 0, s[24:25]
	global_load_lds_dwordx4 v[24:25], off
	v_lshl_add_u64 v[22:23], v[22:23], 0, s[26:27]
	s_add_i32 m0, s34, 0x2000
	s_nop 0
	global_load_lds_dwordx4 v[22:23], off
	s_mov_b32 m0, s69
	v_lshl_add_u64 v[22:23], s[52:53], 0, v[130:131]
	v_lshl_add_u64 v[24:25], v[22:23], 0, s[20:21]
	global_load_lds_dwordx4 v[24:25], off
	v_lshl_add_u64 v[22:23], v[22:23], 0, s[22:23]
	s_mov_b32 m0, s70
	s_nop 0
	global_load_lds_dwordx4 v[22:23], off
	v_add_u32_e32 v172, s72, v1
	ds_read_b128 v[34:37], v172 offset:49152
	ds_read_b128 v[38:41], v172 offset:50176
	ds_read_b128 v[152:155], v172 offset:51200
	ds_read_b128 v[156:159], v172 offset:52224
	ds_read_b128 v[160:163], v172 offset:53248
	ds_read_b128 v[164:167], v172 offset:54272
	ds_read_b128 v[168:171], v172 offset:55296
	ds_read_b128 v[172:175], v172 offset:56320
	s_waitcnt vmcnt(8)
	s_waitcnt lgkmcnt(0)
	s_barrier
	s_setprio 1
	s_waitcnt lgkmcnt(0)
	v_mfma_scale_f32_16x16x128_f8f6f4 v[62:65], v[2:9], v[34:41], v[62:65], v134, v134 op_sel_hi:[0,0,0]
	v_mfma_scale_f32_16x16x128_f8f6f4 v[58:61], v[14:21], v[34:41], v[58:61], v134, v134 op_sel_hi:[0,0,0]
	v_mfma_scale_f32_16x16x128_f8f6f4 v[46:49], v[2:9], v[152:159], v[184:187], v134, v134 op_sel_hi:[0,0,0]
	v_mfma_scale_f32_16x16x128_f8f6f4 v[42:45], v[14:21], v[152:159], v[188:191], v134, v134 op_sel_hi:[0,0,0]
	v_mfma_scale_f32_16x16x128_f8f6f4 v[30:33], v[2:9], v[160:167], v[196:199], v134, v134 op_sel_hi:[0,0,0]
	v_mfma_scale_f32_16x16x128_f8f6f4 v[26:29], v[14:21], v[160:167], v[200:203], v134, v134 op_sel_hi:[0,0,0]
	v_mfma_scale_f32_16x16x128_f8f6f4 v[10:13], v[2:9], v[168:175], v[10:13], v134, v134 op_sel_hi:[0,0,0]
	v_mfma_scale_f32_16x16x128_f8f6f4 v[14:17], v[14:21], v[168:175], v[216:219], v134, v134 op_sel_hi:[0,0,0]
	v_mfma_scale_f32_16x16x128_f8f6f4 v[54:57], v[136:143], v[34:41], v[54:57], v134, v134 op_sel_hi:[0,0,0]
	v_mfma_scale_f32_16x16x128_f8f6f4 v[50:53], v[144:151], v[34:41], v[220:223], v134, v134 op_sel_hi:[0,0,0]
	v_mfma_scale_f32_16x16x128_f8f6f4 v[38:41], v[136:143], v[152:159], v[224:227], v134, v134 op_sel_hi:[0,0,0]
	v_mfma_scale_f32_16x16x128_f8f6f4 v[34:37], v[144:151], v[152:159], v[228:231], v134, v134 op_sel_hi:[0,0,0]
	v_mfma_scale_f32_16x16x128_f8f6f4 v[22:25], v[136:143], v[160:167], v[232:235], v134, v134 op_sel_hi:[0,0,0]
	v_mfma_scale_f32_16x16x128_f8f6f4 v[18:21], v[144:151], v[160:167], v[236:239], v134, v134 op_sel_hi:[0,0,0]
	v_mfma_scale_f32_16x16x128_f8f6f4 v[6:9], v[136:143], v[168:175], v[240:243], v134, v134 op_sel_hi:[0,0,0]
	v_mfma_scale_f32_16x16x128_f8f6f4 v[2:5], v[144:151], v[168:175], v[244:247], v134, v134 op_sel_hi:[0,0,0]
	s_setprio 0
	s_barrier
	s_add_i32 s83, s83, 2
	s_add_u32 s4, s4, 0x100
	s_addc_u32 s5, s5, 0
	s_add_u32 s41, s41, 0x100
	s_addc_u32 s43, s43, 0
	s_cmp_gt_u32 s83, 13
	s_cbranch_scc0 .LBB0_1308
	s_and_b64 vcc, exec, s[28:29]
	s_cbranch_vccz .LBB0_1311
	s_barrier
